# all GEMM K-loops: every load segment issues its ds_read fragment reads first, scalar address arithmetic and DMA issue after them (on top of the gate/up invariant hoist); m1
# baseline (speedup 1.0000x reference)
.LBB0_240:
	ds_read_b128 v[118:121], v210
	ds_read_b128 v[122:125], v210 offset:1024
	ds_read_b128 v[130:133], v210 offset:2048
	ds_read_b128 v[134:137], v210 offset:3072
	ds_read_b128 v[146:149], v211
	ds_read_b128 v[150:153], v211 offset:1024
	ds_read_b128 v[154:157], v211 offset:2048
	ds_read_b128 v[158:161], v211 offset:3072
	ds_read_b128 v[162:165], v212
	ds_read_b128 v[166:169], v212 offset:1024
	ds_read_b128 v[170:173], v212 offset:2048
	ds_read_b128 v[174:177], v212 offset:3072
	ds_read_b128 v[178:181], v212 offset:4096
	ds_read_b128 v[182:185], v212 offset:5120
	ds_read_b128 v[186:189], v212 offset:6144
	ds_read_b128 v[190:193], v212 offset:7168
	s_add_i32 s8, s0, s34
	s_sub_i32 s8, s8, s20
	s_add_i32 s5, s4, s34
	s_add_i32 s18, s8, 0x7ff80
	s_cmp_eq_u32 s3, 28
	s_cselect_b64 s[8:9], -1, 0
	s_and_b64 s[14:15], s[8:9], exec
	s_cselect_b32 s14, 0, s34
	s_mov_b32 m0, s89
	s_nop 0
	buffer_load_dwordx4 v195, s[20:23], s18 offen lds
	s_mov_b32 m0, s90
	s_nop 0
	buffer_load_dwordx4 v205, s[20:23], s18 offen lds
	s_waitcnt vmcnt(8)
	s_waitcnt lgkmcnt(0)
	s_barrier
	v_mfma_f32_16x16x32_bf16 v[142:145], v[118:121], v[162:165], v[142:145]
	v_mfma_f32_16x16x32_bf16 v[138:141], v[130:133], v[162:165], v[138:141]
	v_mfma_f32_16x16x32_bf16 v[110:113], v[118:121], v[170:173], v[110:113]
	v_mfma_f32_16x16x32_bf16 v[106:109], v[130:133], v[170:173], v[106:109]
	v_mfma_f32_16x16x32_bf16 v[94:97], v[118:121], v[178:181], v[94:97]
	v_mfma_f32_16x16x32_bf16 v[90:93], v[130:133], v[178:181], v[90:93]
	v_mfma_f32_16x16x32_bf16 v[78:81], v[118:121], v[186:189], v[78:81]
	v_mfma_f32_16x16x32_bf16 v[74:77], v[130:133], v[186:189], v[74:77]
	v_mfma_f32_16x16x32_bf16 v[126:129], v[146:149], v[162:165], v[126:129]
	v_mfma_f32_16x16x32_bf16 v[114:117], v[154:157], v[162:165], v[114:117]
	v_mfma_f32_16x16x32_bf16 v[102:105], v[146:149], v[170:173], v[102:105]
	v_mfma_f32_16x16x32_bf16 v[98:101], v[154:157], v[170:173], v[98:101]
	v_mfma_f32_16x16x32_bf16 v[86:89], v[146:149], v[178:181], v[86:89]
	v_mfma_f32_16x16x32_bf16 v[82:85], v[154:157], v[178:181], v[82:85]
	v_mfma_f32_16x16x32_bf16 v[70:73], v[146:149], v[186:189], v[70:73]
	v_mfma_f32_16x16x32_bf16 v[66:69], v[154:157], v[186:189], v[66:69]
	v_mfma_f32_16x16x32_bf16 v[142:145], v[122:125], v[166:169], v[142:145]
	v_mfma_f32_16x16x32_bf16 v[138:141], v[134:137], v[166:169], v[138:141]
	v_mfma_f32_16x16x32_bf16 v[110:113], v[122:125], v[174:177], v[110:113]
	v_mfma_f32_16x16x32_bf16 v[106:109], v[134:137], v[174:177], v[106:109]
	v_mfma_f32_16x16x32_bf16 v[94:97], v[122:125], v[182:185], v[94:97]
	v_mfma_f32_16x16x32_bf16 v[90:93], v[134:137], v[182:185], v[90:93]
	v_mfma_f32_16x16x32_bf16 v[78:81], v[122:125], v[190:193], v[78:81]
	v_mfma_f32_16x16x32_bf16 v[74:77], v[134:137], v[190:193], v[74:77]
	v_mfma_f32_16x16x32_bf16 v[126:129], v[150:153], v[166:169], v[126:129]
	v_mfma_f32_16x16x32_bf16 v[114:117], v[158:161], v[166:169], v[114:117]
	v_mfma_f32_16x16x32_bf16 v[102:105], v[150:153], v[174:177], v[102:105]
	v_mfma_f32_16x16x32_bf16 v[98:101], v[158:161], v[174:177], v[98:101]
	v_mfma_f32_16x16x32_bf16 v[86:89], v[150:153], v[182:185], v[86:89]
	v_mfma_f32_16x16x32_bf16 v[82:85], v[158:161], v[182:185], v[82:85]
	v_mfma_f32_16x16x32_bf16 v[70:73], v[150:153], v[190:193], v[70:73]
	v_mfma_f32_16x16x32_bf16 v[66:69], v[158:161], v[190:193], v[66:69]
	s_barrier
	ds_read_b128 v[162:165], v212 offset:16384
	ds_read_b128 v[166:169], v212 offset:17408
	ds_read_b128 v[170:173], v212 offset:18432
	ds_read_b128 v[174:177], v212 offset:19456
	ds_read_b128 v[178:181], v212 offset:20480
	ds_read_b128 v[182:185], v212 offset:21504
	ds_read_b128 v[186:189], v212 offset:22528
	ds_read_b128 v[190:193], v212 offset:23552
	s_cselect_b32 s5, s1, s5
	s_sub_i32 s5, s5, s16
	s_mov_b32 m0, s52
	s_mov_b32 s18, s22
	s_mov_b32 s19, s23
	s_add_i32 s15, s5, 0x80000
	s_and_b64 s[8:9], s[86:87], s[8:9]
	buffer_load_dwordx4 v204, s[16:19], s5 offen lds
	s_mov_b32 m0, s53
	s_and_b64 s[8:9], s[8:9], exec
	buffer_load_dwordx4 v206, s[16:19], s5 offen lds
	s_mov_b32 m0, s54
	s_cselect_b32 s8, s82, s0
	buffer_load_dwordx4 v204, s[16:19], s15 offen lds
	s_mov_b32 m0, s55
	s_add_i32 s8, s8, s14
	buffer_load_dwordx4 v206, s[16:19], s15 offen lds
	s_sub_i32 s8, s8, s20
	s_mov_b32 m0, s33
	s_nop 0
	buffer_load_dwordx4 v195, s[20:23], s8 offen lds
	s_mov_b32 m0, s56
	s_nop 0
	buffer_load_dwordx4 v205, s[20:23], s8 offen lds
	s_waitcnt vmcnt(8)
	s_waitcnt lgkmcnt(0)
	s_barrier
	v_mfma_f32_16x16x32_bf16 v[62:65], v[118:121], v[162:165], v[62:65]
	v_mfma_f32_16x16x32_bf16 v[58:61], v[130:133], v[162:165], v[58:61]
	v_mfma_f32_16x16x32_bf16 v[46:49], v[118:121], v[170:173], v[46:49]
	v_mfma_f32_16x16x32_bf16 v[42:45], v[130:133], v[170:173], v[42:45]
	v_mfma_f32_16x16x32_bf16 v[30:33], v[118:121], v[178:181], v[30:33]
	v_mfma_f32_16x16x32_bf16 v[26:29], v[130:133], v[178:181], v[26:29]
	v_mfma_f32_16x16x32_bf16 v[14:17], v[118:121], v[186:189], v[14:17]
	v_mfma_f32_16x16x32_bf16 v[10:13], v[130:133], v[186:189], v[10:13]
	v_mfma_f32_16x16x32_bf16 v[54:57], v[146:149], v[162:165], v[54:57]
	v_mfma_f32_16x16x32_bf16 v[50:53], v[154:157], v[162:165], v[50:53]
	v_mfma_f32_16x16x32_bf16 v[38:41], v[146:149], v[170:173], v[38:41]
	v_mfma_f32_16x16x32_bf16 v[34:37], v[154:157], v[170:173], v[34:37]
	v_mfma_f32_16x16x32_bf16 v[22:25], v[146:149], v[178:181], v[22:25]
	v_mfma_f32_16x16x32_bf16 v[18:21], v[154:157], v[178:181], v[18:21]
	v_mfma_f32_16x16x32_bf16 v[6:9], v[146:149], v[186:189], v[6:9]
	v_mfma_f32_16x16x32_bf16 v[2:5], v[154:157], v[186:189], v[2:5]
	v_mfma_f32_16x16x32_bf16 v[62:65], v[122:125], v[166:169], v[62:65]
	v_mfma_f32_16x16x32_bf16 v[58:61], v[134:137], v[166:169], v[58:61]
	v_mfma_f32_16x16x32_bf16 v[46:49], v[122:125], v[174:177], v[46:49]
	v_mfma_f32_16x16x32_bf16 v[42:45], v[134:137], v[174:177], v[42:45]
	v_mfma_f32_16x16x32_bf16 v[30:33], v[122:125], v[182:185], v[30:33]
	v_mfma_f32_16x16x32_bf16 v[26:29], v[134:137], v[182:185], v[26:29]
	v_mfma_f32_16x16x32_bf16 v[14:17], v[122:125], v[190:193], v[14:17]
	v_mfma_f32_16x16x32_bf16 v[10:13], v[134:137], v[190:193], v[10:13]
	v_mfma_f32_16x16x32_bf16 v[54:57], v[150:153], v[166:169], v[54:57]
	v_mfma_f32_16x16x32_bf16 v[50:53], v[158:161], v[166:169], v[50:53]
	v_mfma_f32_16x16x32_bf16 v[38:41], v[150:153], v[174:177], v[38:41]
	v_mfma_f32_16x16x32_bf16 v[34:37], v[158:161], v[174:177], v[34:37]
	v_mfma_f32_16x16x32_bf16 v[22:25], v[150:153], v[182:185], v[22:25]
	v_mfma_f32_16x16x32_bf16 v[18:21], v[158:161], v[182:185], v[18:21]
	v_mfma_f32_16x16x32_bf16 v[6:9], v[150:153], v[190:193], v[6:9]
	v_mfma_f32_16x16x32_bf16 v[2:5], v[158:161], v[190:193], v[2:5]
	s_barrier
	ds_read_b128 v[118:121], v213
	ds_read_b128 v[122:125], v213 offset:1024
	ds_read_b128 v[130:133], v213 offset:2048
	ds_read_b128 v[134:137], v213 offset:3072
	ds_read_b128 v[146:149], v214
	ds_read_b128 v[150:153], v214 offset:1024
	ds_read_b128 v[154:157], v214 offset:2048
	ds_read_b128 v[158:161], v214 offset:3072
	ds_read_b128 v[162:165], v212 offset:32768
	ds_read_b128 v[166:169], v212 offset:33792
	ds_read_b128 v[170:173], v212 offset:34816
	ds_read_b128 v[174:177], v212 offset:35840
	ds_read_b128 v[178:181], v212 offset:36864
	ds_read_b128 v[182:185], v212 offset:37888
	ds_read_b128 v[186:189], v212 offset:38912
	ds_read_b128 v[190:193], v212 offset:39936
	s_add_i32 s9, s8, 0x80000
	s_mov_b32 m0, s57
	s_nop 0
	buffer_load_dwordx4 v195, s[20:23], s9 offen lds
	s_mov_b32 m0, s58
	s_nop 0
	buffer_load_dwordx4 v205, s[20:23], s9 offen lds
	s_waitcnt vmcnt(8)
	s_waitcnt lgkmcnt(0)
	s_barrier
	v_mfma_f32_16x16x32_bf16 v[142:145], v[118:121], v[162:165], v[142:145]
	v_mfma_f32_16x16x32_bf16 v[138:141], v[130:133], v[162:165], v[138:141]
	v_mfma_f32_16x16x32_bf16 v[110:113], v[118:121], v[170:173], v[110:113]
	v_mfma_f32_16x16x32_bf16 v[106:109], v[130:133], v[170:173], v[106:109]
	v_mfma_f32_16x16x32_bf16 v[94:97], v[118:121], v[178:181], v[94:97]
	v_mfma_f32_16x16x32_bf16 v[90:93], v[130:133], v[178:181], v[90:93]
	v_mfma_f32_16x16x32_bf16 v[78:81], v[118:121], v[186:189], v[78:81]
	v_mfma_f32_16x16x32_bf16 v[74:77], v[130:133], v[186:189], v[74:77]
	v_mfma_f32_16x16x32_bf16 v[126:129], v[146:149], v[162:165], v[126:129]
	v_mfma_f32_16x16x32_bf16 v[114:117], v[154:157], v[162:165], v[114:117]
	v_mfma_f32_16x16x32_bf16 v[102:105], v[146:149], v[170:173], v[102:105]
	v_mfma_f32_16x16x32_bf16 v[98:101], v[154:157], v[170:173], v[98:101]
	v_mfma_f32_16x16x32_bf16 v[86:89], v[146:149], v[178:181], v[86:89]
	v_mfma_f32_16x16x32_bf16 v[82:85], v[154:157], v[178:181], v[82:85]
	v_mfma_f32_16x16x32_bf16 v[70:73], v[146:149], v[186:189], v[70:73]
	v_mfma_f32_16x16x32_bf16 v[66:69], v[154:157], v[186:189], v[66:69]
	v_mfma_f32_16x16x32_bf16 v[142:145], v[122:125], v[166:169], v[142:145]
	v_mfma_f32_16x16x32_bf16 v[138:141], v[134:137], v[166:169], v[138:141]
	v_mfma_f32_16x16x32_bf16 v[110:113], v[122:125], v[174:177], v[110:113]
	v_mfma_f32_16x16x32_bf16 v[106:109], v[134:137], v[174:177], v[106:109]
	v_mfma_f32_16x16x32_bf16 v[94:97], v[122:125], v[182:185], v[94:97]
	v_mfma_f32_16x16x32_bf16 v[90:93], v[134:137], v[182:185], v[90:93]
	v_mfma_f32_16x16x32_bf16 v[78:81], v[122:125], v[190:193], v[78:81]
	v_mfma_f32_16x16x32_bf16 v[74:77], v[134:137], v[190:193], v[74:77]
	v_mfma_f32_16x16x32_bf16 v[126:129], v[150:153], v[166:169], v[126:129]
	v_mfma_f32_16x16x32_bf16 v[114:117], v[158:161], v[166:169], v[114:117]
	v_mfma_f32_16x16x32_bf16 v[102:105], v[150:153], v[174:177], v[102:105]
	v_mfma_f32_16x16x32_bf16 v[98:101], v[158:161], v[174:177], v[98:101]
	v_mfma_f32_16x16x32_bf16 v[86:89], v[150:153], v[182:185], v[86:89]
	v_mfma_f32_16x16x32_bf16 v[82:85], v[158:161], v[182:185], v[82:85]
	v_mfma_f32_16x16x32_bf16 v[70:73], v[150:153], v[190:193], v[70:73]
	v_mfma_f32_16x16x32_bf16 v[66:69], v[158:161], v[190:193], v[66:69]
	s_barrier
	ds_read_b128 v[162:165], v212 offset:49152
	ds_read_b128 v[166:169], v212 offset:50176
	ds_read_b128 v[170:173], v212 offset:51200
	ds_read_b128 v[174:177], v212 offset:52224
	ds_read_b128 v[178:181], v212 offset:53248
	ds_read_b128 v[182:185], v212 offset:54272
	ds_read_b128 v[186:189], v212 offset:55296
	ds_read_b128 v[190:193], v212 offset:56320
	s_mov_b32 m0, s62
	s_add_i32 s9, s5, 0x80
	buffer_load_dwordx4 v204, s[16:19], s9 offen lds
	s_mov_b32 m0, s63
	s_add_i32 s5, s5, 0x80080
	buffer_load_dwordx4 v206, s[16:19], s9 offen lds
	s_mov_b32 m0, s75
	s_addk_i32 s8, 0x80
	buffer_load_dwordx4 v204, s[16:19], s5 offen lds
	s_mov_b32 m0, s88
	s_nop 0
	buffer_load_dwordx4 v206, s[16:19], s5 offen lds
	s_mov_b32 m0, s68
	s_nop 0
	buffer_load_dwordx4 v195, s[20:23], s8 offen lds
	s_mov_b32 m0, s69
	s_nop 0
	buffer_load_dwordx4 v205, s[20:23], s8 offen lds
	s_waitcnt vmcnt(8)
	s_waitcnt lgkmcnt(0)
	s_barrier
	v_mfma_f32_16x16x32_bf16 v[62:65], v[118:121], v[162:165], v[62:65]
	v_mfma_f32_16x16x32_bf16 v[58:61], v[130:133], v[162:165], v[58:61]
	v_mfma_f32_16x16x32_bf16 v[46:49], v[118:121], v[170:173], v[46:49]
	v_mfma_f32_16x16x32_bf16 v[42:45], v[130:133], v[170:173], v[42:45]
	v_mfma_f32_16x16x32_bf16 v[30:33], v[118:121], v[178:181], v[30:33]
	v_mfma_f32_16x16x32_bf16 v[26:29], v[130:133], v[178:181], v[26:29]
	v_mfma_f32_16x16x32_bf16 v[14:17], v[118:121], v[186:189], v[14:17]
	v_mfma_f32_16x16x32_bf16 v[10:13], v[130:133], v[186:189], v[10:13]
	v_mfma_f32_16x16x32_bf16 v[54:57], v[146:149], v[162:165], v[54:57]
	v_mfma_f32_16x16x32_bf16 v[50:53], v[154:157], v[162:165], v[50:53]
	v_mfma_f32_16x16x32_bf16 v[38:41], v[146:149], v[170:173], v[38:41]
	v_mfma_f32_16x16x32_bf16 v[34:37], v[154:157], v[170:173], v[34:37]
	v_mfma_f32_16x16x32_bf16 v[22:25], v[146:149], v[178:181], v[22:25]
	v_mfma_f32_16x16x32_bf16 v[18:21], v[154:157], v[178:181], v[18:21]
	v_mfma_f32_16x16x32_bf16 v[6:9], v[146:149], v[186:189], v[6:9]
	v_mfma_f32_16x16x32_bf16 v[2:5], v[154:157], v[186:189], v[2:5]
	v_mfma_f32_16x16x32_bf16 v[62:65], v[122:125], v[166:169], v[62:65]
	v_mfma_f32_16x16x32_bf16 v[58:61], v[134:137], v[166:169], v[58:61]
	v_mfma_f32_16x16x32_bf16 v[46:49], v[122:125], v[174:177], v[46:49]
	v_mfma_f32_16x16x32_bf16 v[42:45], v[134:137], v[174:177], v[42:45]
	v_mfma_f32_16x16x32_bf16 v[30:33], v[122:125], v[182:185], v[30:33]
	v_mfma_f32_16x16x32_bf16 v[26:29], v[134:137], v[182:185], v[26:29]
	v_mfma_f32_16x16x32_bf16 v[14:17], v[122:125], v[190:193], v[14:17]
	v_mfma_f32_16x16x32_bf16 v[10:13], v[134:137], v[190:193], v[10:13]
	v_mfma_f32_16x16x32_bf16 v[54:57], v[150:153], v[166:169], v[54:57]
	v_mfma_f32_16x16x32_bf16 v[50:53], v[158:161], v[166:169], v[50:53]
	v_mfma_f32_16x16x32_bf16 v[38:41], v[150:153], v[174:177], v[38:41]
	v_mfma_f32_16x16x32_bf16 v[34:37], v[158:161], v[174:177], v[34:37]
	v_mfma_f32_16x16x32_bf16 v[22:25], v[150:153], v[182:185], v[22:25]
	v_mfma_f32_16x16x32_bf16 v[18:21], v[158:161], v[182:185], v[18:21]
	v_mfma_f32_16x16x32_bf16 v[6:9], v[150:153], v[190:193], v[6:9]
	v_mfma_f32_16x16x32_bf16 v[2:5], v[158:161], v[190:193], v[2:5]
	s_barrier
	s_add_i32 s3, s3, 2
	s_add_u32 s34, s34, 0x100
	s_addc_u32 s35, s35, 0
	s_cmp_lt_u32 s3, 30
	s_cbranch_scc1 .LBB0_240
	s_andn2_b64 vcc, exec, s[70:71]
	s_cbranch_vccnz .LBB0_243
	s_barrier

.LBB0_816:
	ds_read_b128 v[132:135], v148
	ds_read_b128 v[136:139], v148 offset:1024
	ds_read_b128 v[154:157], v148 offset:2048
	ds_read_b128 v[158:161], v148 offset:3072
	ds_read_b128 v[162:165], v149
	ds_read_b128 v[166:169], v149 offset:1024
	ds_read_b128 v[170:173], v149 offset:2048
	ds_read_b128 v[174:177], v149 offset:3072
	ds_read_b128 v[178:181], v150
	ds_read_b128 v[182:185], v150 offset:1024
	ds_read_b128 v[186:189], v150 offset:2048
	ds_read_b128 v[190:193], v150 offset:3072
	ds_read_b128 v[196:199], v150 offset:4096
	ds_read_b128 v[200:203], v150 offset:5120
	ds_read_b128 v[204:207], v150 offset:6144
	ds_read_b128 v[208:211], v150 offset:7168
	s_add_i32 s6, s36, s44
	s_sub_i32 s6, s6, s16
	s_add_i32 s14, s38, s44
	s_add_i32 s15, s6, 0x7ff80
	s_cmp_eq_u32 s25, 28
	s_cselect_b64 s[8:9], -1, 0
	s_and_b64 s[6:7], s[8:9], exec
	s_cselect_b32 s37, 0, s44
	s_mov_b32 m0, s67
	s_nop 0
	buffer_load_dwordx4 v142, s[16:19], s15 offen lds
	s_mov_b32 m0, s68
	s_nop 0
	buffer_load_dwordx4 v144, s[16:19], s15 offen lds
	s_waitcnt vmcnt(8)
	s_waitcnt lgkmcnt(0)
	s_barrier
	v_mfma_f32_16x16x32_bf16 v[126:129], v[132:135], v[178:181], v[126:129]
	v_mfma_f32_16x16x32_bf16 v[122:125], v[154:157], v[178:181], v[122:125]
	v_mfma_f32_16x16x32_bf16 v[118:121], v[132:135], v[186:189], v[118:121]
	v_mfma_f32_16x16x32_bf16 v[114:117], v[154:157], v[186:189], v[114:117]
	v_mfma_f32_16x16x32_bf16 v[98:101], v[132:135], v[196:199], v[98:101]
	v_mfma_f32_16x16x32_bf16 v[90:93], v[154:157], v[196:199], v[90:93]
	v_mfma_f32_16x16x32_bf16 v[82:85], v[132:135], v[204:207], v[82:85]
	v_mfma_f32_16x16x32_bf16 v[74:77], v[154:157], v[204:207], v[74:77]
	v_mfma_f32_16x16x32_bf16 v[110:113], v[162:165], v[178:181], v[110:113]
	v_mfma_f32_16x16x32_bf16 v[106:109], v[170:173], v[178:181], v[106:109]
	v_mfma_f32_16x16x32_bf16 v[102:105], v[162:165], v[186:189], v[102:105]
	v_mfma_f32_16x16x32_bf16 v[94:97], v[170:173], v[186:189], v[94:97]
	v_mfma_f32_16x16x32_bf16 v[86:89], v[162:165], v[196:199], v[86:89]
	v_mfma_f32_16x16x32_bf16 v[78:81], v[170:173], v[196:199], v[78:81]
	v_mfma_f32_16x16x32_bf16 v[70:73], v[162:165], v[204:207], v[70:73]
	v_mfma_f32_16x16x32_bf16 v[66:69], v[170:173], v[204:207], v[66:69]
	v_mfma_f32_16x16x32_bf16 v[126:129], v[136:139], v[182:185], v[126:129]
	v_mfma_f32_16x16x32_bf16 v[122:125], v[158:161], v[182:185], v[122:125]
	v_mfma_f32_16x16x32_bf16 v[118:121], v[136:139], v[190:193], v[118:121]
	v_mfma_f32_16x16x32_bf16 v[114:117], v[158:161], v[190:193], v[114:117]
	v_mfma_f32_16x16x32_bf16 v[98:101], v[136:139], v[200:203], v[98:101]
	v_mfma_f32_16x16x32_bf16 v[90:93], v[158:161], v[200:203], v[90:93]
	v_mfma_f32_16x16x32_bf16 v[82:85], v[136:139], v[208:211], v[82:85]
	v_mfma_f32_16x16x32_bf16 v[74:77], v[158:161], v[208:211], v[74:77]
	v_mfma_f32_16x16x32_bf16 v[110:113], v[166:169], v[182:185], v[110:113]
	v_mfma_f32_16x16x32_bf16 v[106:109], v[174:177], v[182:185], v[106:109]
	v_mfma_f32_16x16x32_bf16 v[102:105], v[166:169], v[190:193], v[102:105]
	v_mfma_f32_16x16x32_bf16 v[94:97], v[174:177], v[190:193], v[94:97]
	v_mfma_f32_16x16x32_bf16 v[86:89], v[166:169], v[200:203], v[86:89]
	v_mfma_f32_16x16x32_bf16 v[78:81], v[174:177], v[200:203], v[78:81]
	v_mfma_f32_16x16x32_bf16 v[70:73], v[166:169], v[208:211], v[70:73]
	v_mfma_f32_16x16x32_bf16 v[66:69], v[174:177], v[208:211], v[66:69]
	s_barrier
	ds_read_b128 v[178:181], v150 offset:16384
	ds_read_b128 v[182:185], v150 offset:17408
	ds_read_b128 v[186:189], v150 offset:18432
	ds_read_b128 v[190:193], v150 offset:19456
	ds_read_b128 v[196:199], v150 offset:20480
	ds_read_b128 v[200:203], v150 offset:21504
	ds_read_b128 v[204:207], v150 offset:22528
	ds_read_b128 v[208:211], v150 offset:23552
	s_cselect_b32 s14, s23, s14
	s_sub_i32 s14, s14, s4
	s_mov_b32 m0, s52
	s_mov_b32 s6, s18
	s_mov_b32 s7, s19
	s_add_i32 s15, s14, 0x80000
	s_and_b64 s[8:9], s[30:31], s[8:9]
	buffer_load_dwordx4 v143, s[4:7], s14 offen lds
	s_mov_b32 m0, s53
	s_and_b64 s[8:9], s[8:9], exec
	buffer_load_dwordx4 v145, s[4:7], s14 offen lds
	s_mov_b32 m0, s54
	s_cselect_b32 s8, s26, s36
	buffer_load_dwordx4 v143, s[4:7], s15 offen lds
	s_mov_b32 m0, s55
	s_add_i32 s8, s8, s37
	buffer_load_dwordx4 v145, s[4:7], s15 offen lds
	s_sub_i32 s8, s8, s16
	s_mov_b32 m0, s35
	s_nop 0
	buffer_load_dwordx4 v142, s[16:19], s8 offen lds
	s_mov_b32 m0, s56
	s_nop 0
	buffer_load_dwordx4 v144, s[16:19], s8 offen lds
	s_waitcnt vmcnt(8)
	s_waitcnt lgkmcnt(0)
	s_barrier
	v_mfma_f32_16x16x32_bf16 v[62:65], v[132:135], v[178:181], v[62:65]
	v_mfma_f32_16x16x32_bf16 v[58:61], v[154:157], v[178:181], v[58:61]
	v_mfma_f32_16x16x32_bf16 v[54:57], v[132:135], v[186:189], v[54:57]
	v_mfma_f32_16x16x32_bf16 v[46:49], v[154:157], v[186:189], v[46:49]
	v_mfma_f32_16x16x32_bf16 v[38:41], v[132:135], v[196:199], v[38:41]
	v_mfma_f32_16x16x32_bf16 v[30:33], v[154:157], v[196:199], v[30:33]
	v_mfma_f32_16x16x32_bf16 v[22:25], v[132:135], v[204:207], v[22:25]
	v_mfma_f32_16x16x32_bf16 v[14:17], v[154:157], v[204:207], v[14:17]
	v_mfma_f32_16x16x32_bf16 v[50:53], v[162:165], v[178:181], v[50:53]
	v_mfma_f32_16x16x32_bf16 v[42:45], v[170:173], v[178:181], v[42:45]
	v_mfma_f32_16x16x32_bf16 v[34:37], v[162:165], v[186:189], v[34:37]
	v_mfma_f32_16x16x32_bf16 v[26:29], v[170:173], v[186:189], v[26:29]
	v_mfma_f32_16x16x32_bf16 v[18:21], v[162:165], v[196:199], v[18:21]
	v_mfma_f32_16x16x32_bf16 v[10:13], v[170:173], v[196:199], v[10:13]
	v_mfma_f32_16x16x32_bf16 v[6:9], v[162:165], v[204:207], v[6:9]
	v_mfma_f32_16x16x32_bf16 v[2:5], v[170:173], v[204:207], v[2:5]
	v_mfma_f32_16x16x32_bf16 v[62:65], v[136:139], v[182:185], v[62:65]
	v_mfma_f32_16x16x32_bf16 v[58:61], v[158:161], v[182:185], v[58:61]
	v_mfma_f32_16x16x32_bf16 v[54:57], v[136:139], v[190:193], v[54:57]
	v_mfma_f32_16x16x32_bf16 v[46:49], v[158:161], v[190:193], v[46:49]
	v_mfma_f32_16x16x32_bf16 v[38:41], v[136:139], v[200:203], v[38:41]
	v_mfma_f32_16x16x32_bf16 v[30:33], v[158:161], v[200:203], v[30:33]
	v_mfma_f32_16x16x32_bf16 v[22:25], v[136:139], v[208:211], v[22:25]
	v_mfma_f32_16x16x32_bf16 v[14:17], v[158:161], v[208:211], v[14:17]
	v_mfma_f32_16x16x32_bf16 v[50:53], v[166:169], v[182:185], v[50:53]
	v_mfma_f32_16x16x32_bf16 v[42:45], v[174:177], v[182:185], v[42:45]
	v_mfma_f32_16x16x32_bf16 v[34:37], v[166:169], v[190:193], v[34:37]
	v_mfma_f32_16x16x32_bf16 v[26:29], v[174:177], v[190:193], v[26:29]
	v_mfma_f32_16x16x32_bf16 v[18:21], v[166:169], v[200:203], v[18:21]
	v_mfma_f32_16x16x32_bf16 v[10:13], v[174:177], v[200:203], v[10:13]
	v_mfma_f32_16x16x32_bf16 v[6:9], v[166:169], v[208:211], v[6:9]
	v_mfma_f32_16x16x32_bf16 v[2:5], v[174:177], v[208:211], v[2:5]
	s_barrier
	ds_read_b128 v[132:135], v151
	ds_read_b128 v[136:139], v151 offset:1024
	ds_read_b128 v[154:157], v151 offset:2048
	ds_read_b128 v[158:161], v151 offset:3072
	ds_read_b128 v[162:165], v152
	ds_read_b128 v[166:169], v152 offset:1024
	ds_read_b128 v[170:173], v152 offset:2048
	ds_read_b128 v[174:177], v152 offset:3072
	ds_read_b128 v[178:181], v150 offset:32768
	ds_read_b128 v[182:185], v150 offset:33792
	ds_read_b128 v[186:189], v150 offset:34816
	ds_read_b128 v[190:193], v150 offset:35840
	ds_read_b128 v[196:199], v150 offset:36864
	ds_read_b128 v[200:203], v150 offset:37888
	ds_read_b128 v[204:207], v150 offset:38912
	ds_read_b128 v[208:211], v150 offset:39936
	s_add_i32 s9, s8, 0x80000
	s_mov_b32 m0, s57
	s_nop 0
	buffer_load_dwordx4 v142, s[16:19], s9 offen lds
	s_mov_b32 m0, s58
	s_nop 0
	buffer_load_dwordx4 v144, s[16:19], s9 offen lds
	s_waitcnt vmcnt(8)
	s_waitcnt lgkmcnt(0)
	s_barrier
	v_mfma_f32_16x16x32_bf16 v[126:129], v[132:135], v[178:181], v[126:129]
	v_mfma_f32_16x16x32_bf16 v[122:125], v[154:157], v[178:181], v[122:125]
	v_mfma_f32_16x16x32_bf16 v[118:121], v[132:135], v[186:189], v[118:121]
	v_mfma_f32_16x16x32_bf16 v[114:117], v[154:157], v[186:189], v[114:117]
	v_mfma_f32_16x16x32_bf16 v[98:101], v[132:135], v[196:199], v[98:101]
	v_mfma_f32_16x16x32_bf16 v[90:93], v[154:157], v[196:199], v[90:93]
	v_mfma_f32_16x16x32_bf16 v[82:85], v[132:135], v[204:207], v[82:85]
	v_mfma_f32_16x16x32_bf16 v[74:77], v[154:157], v[204:207], v[74:77]
	v_mfma_f32_16x16x32_bf16 v[110:113], v[162:165], v[178:181], v[110:113]
	v_mfma_f32_16x16x32_bf16 v[106:109], v[170:173], v[178:181], v[106:109]
	v_mfma_f32_16x16x32_bf16 v[102:105], v[162:165], v[186:189], v[102:105]
	v_mfma_f32_16x16x32_bf16 v[94:97], v[170:173], v[186:189], v[94:97]
	v_mfma_f32_16x16x32_bf16 v[86:89], v[162:165], v[196:199], v[86:89]
	v_mfma_f32_16x16x32_bf16 v[78:81], v[170:173], v[196:199], v[78:81]
	v_mfma_f32_16x16x32_bf16 v[70:73], v[162:165], v[204:207], v[70:73]
	v_mfma_f32_16x16x32_bf16 v[66:69], v[170:173], v[204:207], v[66:69]
	v_mfma_f32_16x16x32_bf16 v[126:129], v[136:139], v[182:185], v[126:129]
	v_mfma_f32_16x16x32_bf16 v[122:125], v[158:161], v[182:185], v[122:125]
	v_mfma_f32_16x16x32_bf16 v[118:121], v[136:139], v[190:193], v[118:121]
	v_mfma_f32_16x16x32_bf16 v[114:117], v[158:161], v[190:193], v[114:117]
	v_mfma_f32_16x16x32_bf16 v[98:101], v[136:139], v[200:203], v[98:101]
	v_mfma_f32_16x16x32_bf16 v[90:93], v[158:161], v[200:203], v[90:93]
	v_mfma_f32_16x16x32_bf16 v[82:85], v[136:139], v[208:211], v[82:85]
	v_mfma_f32_16x16x32_bf16 v[74:77], v[158:161], v[208:211], v[74:77]
	v_mfma_f32_16x16x32_bf16 v[110:113], v[166:169], v[182:185], v[110:113]
	v_mfma_f32_16x16x32_bf16 v[106:109], v[174:177], v[182:185], v[106:109]
	v_mfma_f32_16x16x32_bf16 v[102:105], v[166:169], v[190:193], v[102:105]
	v_mfma_f32_16x16x32_bf16 v[94:97], v[174:177], v[190:193], v[94:97]
	v_mfma_f32_16x16x32_bf16 v[86:89], v[166:169], v[200:203], v[86:89]
	v_mfma_f32_16x16x32_bf16 v[78:81], v[174:177], v[200:203], v[78:81]
	v_mfma_f32_16x16x32_bf16 v[70:73], v[166:169], v[208:211], v[70:73]
	v_mfma_f32_16x16x32_bf16 v[66:69], v[174:177], v[208:211], v[66:69]
	s_barrier
	ds_read_b128 v[178:181], v150 offset:49152
	ds_read_b128 v[182:185], v150 offset:50176
	ds_read_b128 v[186:189], v150 offset:51200
	ds_read_b128 v[190:193], v150 offset:52224
	ds_read_b128 v[196:199], v150 offset:53248
	ds_read_b128 v[200:203], v150 offset:54272
	ds_read_b128 v[204:207], v150 offset:55296
	ds_read_b128 v[208:211], v150 offset:56320
	s_mov_b32 m0, s61
	s_add_i32 s9, s14, 0x80
	buffer_load_dwordx4 v143, s[4:7], s9 offen lds
	s_mov_b32 m0, s62
	s_add_i32 s14, s14, 0x80080
	buffer_load_dwordx4 v145, s[4:7], s9 offen lds
	s_mov_b32 m0, s65
	s_addk_i32 s8, 0x80
	buffer_load_dwordx4 v143, s[4:7], s14 offen lds
	s_mov_b32 m0, s66
	s_nop 0
	buffer_load_dwordx4 v145, s[4:7], s14 offen lds
	s_mov_b32 m0, s63
	s_nop 0
	buffer_load_dwordx4 v142, s[16:19], s8 offen lds
	s_mov_b32 m0, s64
	s_nop 0
	buffer_load_dwordx4 v144, s[16:19], s8 offen lds
	s_waitcnt vmcnt(8)
	s_waitcnt lgkmcnt(0)
	s_barrier
	v_mfma_f32_16x16x32_bf16 v[62:65], v[132:135], v[178:181], v[62:65]
	v_mfma_f32_16x16x32_bf16 v[58:61], v[154:157], v[178:181], v[58:61]
	v_mfma_f32_16x16x32_bf16 v[54:57], v[132:135], v[186:189], v[54:57]
	v_mfma_f32_16x16x32_bf16 v[46:49], v[154:157], v[186:189], v[46:49]
	v_mfma_f32_16x16x32_bf16 v[38:41], v[132:135], v[196:199], v[38:41]
	v_mfma_f32_16x16x32_bf16 v[30:33], v[154:157], v[196:199], v[30:33]
	v_mfma_f32_16x16x32_bf16 v[22:25], v[132:135], v[204:207], v[22:25]
	v_mfma_f32_16x16x32_bf16 v[14:17], v[154:157], v[204:207], v[14:17]
	v_mfma_f32_16x16x32_bf16 v[50:53], v[162:165], v[178:181], v[50:53]
	v_mfma_f32_16x16x32_bf16 v[42:45], v[170:173], v[178:181], v[42:45]
	v_mfma_f32_16x16x32_bf16 v[34:37], v[162:165], v[186:189], v[34:37]
	v_mfma_f32_16x16x32_bf16 v[26:29], v[170:173], v[186:189], v[26:29]
	v_mfma_f32_16x16x32_bf16 v[18:21], v[162:165], v[196:199], v[18:21]
	v_mfma_f32_16x16x32_bf16 v[10:13], v[170:173], v[196:199], v[10:13]
	v_mfma_f32_16x16x32_bf16 v[6:9], v[162:165], v[204:207], v[6:9]
	v_mfma_f32_16x16x32_bf16 v[2:5], v[170:173], v[204:207], v[2:5]
	v_mfma_f32_16x16x32_bf16 v[62:65], v[136:139], v[182:185], v[62:65]
	v_mfma_f32_16x16x32_bf16 v[58:61], v[158:161], v[182:185], v[58:61]
	v_mfma_f32_16x16x32_bf16 v[54:57], v[136:139], v[190:193], v[54:57]
	v_mfma_f32_16x16x32_bf16 v[46:49], v[158:161], v[190:193], v[46:49]
	v_mfma_f32_16x16x32_bf16 v[38:41], v[136:139], v[200:203], v[38:41]
	v_mfma_f32_16x16x32_bf16 v[30:33], v[158:161], v[200:203], v[30:33]
	v_mfma_f32_16x16x32_bf16 v[22:25], v[136:139], v[208:211], v[22:25]
	v_mfma_f32_16x16x32_bf16 v[14:17], v[158:161], v[208:211], v[14:17]
	v_mfma_f32_16x16x32_bf16 v[50:53], v[166:169], v[182:185], v[50:53]
	v_mfma_f32_16x16x32_bf16 v[42:45], v[174:177], v[182:185], v[42:45]
	v_mfma_f32_16x16x32_bf16 v[34:37], v[166:169], v[190:193], v[34:37]
	v_mfma_f32_16x16x32_bf16 v[26:29], v[174:177], v[190:193], v[26:29]
	v_mfma_f32_16x16x32_bf16 v[18:21], v[166:169], v[200:203], v[18:21]
	v_mfma_f32_16x16x32_bf16 v[10:13], v[174:177], v[200:203], v[10:13]
	v_mfma_f32_16x16x32_bf16 v[6:9], v[166:169], v[208:211], v[6:9]
	v_mfma_f32_16x16x32_bf16 v[2:5], v[174:177], v[208:211], v[2:5]
	s_barrier
	s_add_i32 s25, s25, 2
	s_add_u32 s44, s44, 0x100
	s_addc_u32 s45, s45, 0
	s_cmp_lt_u32 s25, 30
	s_cbranch_scc1 .LBB0_816
	s_andn2_b64 vcc, exec, s[20:21]
	s_cbranch_vccnz .LBB0_819
	s_barrier

.LBB0_1238:
	v_add_u32_e32 v137, 0, v157
	v_add_u32_e32 v30, 0x10000, v137
	v_add_u32_e32 v62, 0x14000, v137
	ds_read_b128 v[6:9], v30
	ds_read_b128 v[14:17], v30 offset:1024
	ds_read_b128 v[18:21], v30 offset:2048
	ds_read_b128 v[30:33], v30 offset:3072
	ds_read_b128 v[34:37], v62
	ds_read_b128 v[46:49], v62 offset:1024
	ds_read_b128 v[50:53], v62 offset:2048
	ds_read_b128 v[62:65], v62 offset:3072
	v_add_u32_e32 v153, 0, v156
	ds_read_b128 v[66:69], v153
	ds_read_b128 v[78:81], v153 offset:1024
	ds_read_b128 v[82:85], v153 offset:2048
	ds_read_b128 v[94:97], v153 offset:3072
	ds_read_b128 v[98:101], v153 offset:4096
	ds_read_b128 v[106:109], v153 offset:5120
	ds_read_b128 v[114:117], v153 offset:6144
	ds_read_b128 v[138:141], v153 offset:7168
	s_add_u32 s42, s18, 0x100
	s_addc_u32 s43, s19, 0
	s_add_i32 s85, s29, s18
	s_and_b64 s[14:15], s[44:45], exec
	s_cselect_b32 s86, 0, s42
	s_add_i32 s14, s18, 0x80
	s_mov_b32 m0, s79
	s_nop 0
	buffer_load_dwordx4 v132, s[8:11], s14 offen lds
	s_mov_b32 m0, s80
	s_nop 0
	buffer_load_dwordx4 v134, s[8:11], s14 offen lds
	s_waitcnt vmcnt(8)
	s_waitcnt lgkmcnt(0)
	s_barrier
	v_mfma_f32_16x16x32_bf16 v[126:129], v[6:9], v[66:69], v[126:129]
	v_mfma_f32_16x16x32_bf16 v[102:105], v[6:9], v[82:85], v[102:105]
	v_mfma_f32_16x16x32_bf16 v[70:73], v[6:9], v[98:101], v[70:73]
	v_mfma_f32_16x16x32_bf16 v[6:9], v[6:9], v[114:117], v[38:41]
	v_mfma_f32_16x16x32_bf16 v[126:129], v[14:17], v[78:81], v[126:129]
	v_mfma_f32_16x16x32_bf16 v[122:125], v[18:21], v[66:69], v[122:125]
	v_mfma_f32_16x16x32_bf16 v[102:105], v[14:17], v[94:97], v[102:105]
	v_mfma_f32_16x16x32_bf16 v[90:93], v[18:21], v[82:85], v[90:93]
	v_mfma_f32_16x16x32_bf16 v[70:73], v[14:17], v[106:109], v[70:73]
	v_mfma_f32_16x16x32_bf16 v[58:61], v[18:21], v[98:101], v[58:61]
	v_mfma_f32_16x16x32_bf16 v[6:9], v[14:17], v[138:141], v[6:9]
	v_mfma_f32_16x16x32_bf16 v[14:17], v[18:21], v[114:117], v[26:29]
	v_mfma_f32_16x16x32_bf16 v[26:29], v[50:53], v[66:69], v[110:113]
	v_mfma_f32_16x16x32_bf16 v[122:125], v[30:33], v[78:81], v[122:125]
	v_mfma_f32_16x16x32_bf16 v[90:93], v[30:33], v[94:97], v[90:93]
	v_mfma_f32_16x16x32_bf16 v[58:61], v[30:33], v[106:109], v[58:61]
	v_mfma_f32_16x16x32_bf16 v[14:17], v[30:33], v[138:141], v[14:17]
	v_mfma_f32_16x16x32_bf16 v[30:33], v[62:65], v[78:81], v[26:29]
	v_mfma_f32_16x16x32_bf16 v[26:29], v[34:37], v[82:85], v[86:89]
	v_mfma_f32_16x16x32_bf16 v[18:21], v[34:37], v[66:69], v[118:121]
	v_mfma_f32_16x16x32_bf16 v[66:69], v[46:49], v[94:97], v[26:29]
	v_mfma_f32_16x16x32_bf16 v[26:29], v[50:53], v[82:85], v[74:77]
	v_mfma_f32_16x16x32_bf16 v[74:77], v[62:65], v[94:97], v[26:29]
	v_mfma_f32_16x16x32_bf16 v[26:29], v[34:37], v[98:101], v[54:57]
	v_mfma_f32_16x16x32_bf16 v[54:57], v[46:49], v[106:109], v[26:29]
	v_mfma_f32_16x16x32_bf16 v[26:29], v[50:53], v[98:101], v[42:45]
	v_mfma_f32_16x16x32_bf16 v[22:25], v[34:37], v[114:117], v[22:25]
	v_mfma_f32_16x16x32_bf16 v[10:13], v[50:53], v[114:117], v[10:13]
	v_mfma_f32_16x16x32_bf16 v[42:45], v[62:65], v[106:109], v[26:29]
	v_mfma_f32_16x16x32_bf16 v[22:25], v[46:49], v[138:141], v[22:25]
	v_mfma_f32_16x16x32_bf16 v[10:13], v[62:65], v[138:141], v[10:13]
	v_mfma_f32_16x16x32_bf16 v[18:21], v[46:49], v[78:81], v[18:21]
	s_barrier
	s_and_b64 s[14:15], s[44:45], exec
	s_cselect_b32 s14, s5, s85
	s_mov_b32 m0, s66
	s_mov_b32 s18, s10
	s_mov_b32 s19, s11
	s_sub_i32 s14, s14, s16
	buffer_load_dwordx4 v151, s[16:19], s14 offen lds
	s_mov_b32 m0, s67
	s_add_i32 s15, s14, 0x80000
	buffer_load_dwordx4 v158, s[16:19], s14 offen lds
	s_mov_b32 m0, s68
	s_nop 0
	buffer_load_dwordx4 v151, s[16:19], s15 offen lds
	s_mov_b32 m0, s69
	s_nop 0
	buffer_load_dwordx4 v158, s[16:19], s15 offen lds
	s_mov_b32 m0, s65
	s_nop 0
	buffer_load_dwordx4 v3, s[8:11], s86 offen lds
	s_mov_b32 m0, s70
	s_nop 0
	buffer_load_dwordx4 v2, s[8:11], s86 offen lds
	s_waitcnt vmcnt(8)
	s_waitcnt lgkmcnt(0)
	s_barrier
	s_barrier
	v_add_u32_e32 v38, 0x18000, v137
	ds_read_b128 v[26:29], v38
	ds_read_b128 v[34:37], v38 offset:1024
	ds_read_b128 v[46:49], v38 offset:2048
	ds_read_b128 v[50:53], v38 offset:3072
	v_add_u32_e32 v38, 0x1c000, v137
	ds_read_b128 v[62:65], v38
	ds_read_b128 v[78:81], v38 offset:1024
	ds_read_b128 v[82:85], v38 offset:2048
	ds_read_b128 v[94:97], v38 offset:3072
	ds_read_b128 v[86:89], v153 offset:32768
	ds_read_b128 v[98:101], v153 offset:33792
	ds_read_b128 v[106:109], v153 offset:34816
	ds_read_b128 v[114:117], v153 offset:35840
	ds_read_b128 v[138:141], v153 offset:36864
	ds_read_b128 v[142:145], v153 offset:37888
	ds_read_b128 v[172:175], v153 offset:38912
	ds_read_b128 v[176:179], v153 offset:39936
	s_mov_b32 m0, s71
	s_nop 0
	buffer_load_dwordx4 v5, s[8:11], s86 offen lds
	s_mov_b32 m0, s72
	s_nop 0
	buffer_load_dwordx4 v4, s[8:11], s86 offen lds
	s_waitcnt vmcnt(8)
	s_waitcnt lgkmcnt(0)
	s_barrier
	v_mfma_f32_16x16x32_bf16 v[38:41], v[26:29], v[86:89], v[126:129]
	v_mfma_f32_16x16x32_bf16 v[126:129], v[34:37], v[98:101], v[38:41]
	v_mfma_f32_16x16x32_bf16 v[38:41], v[46:49], v[86:89], v[122:125]
	v_mfma_f32_16x16x32_bf16 v[122:125], v[50:53], v[98:101], v[38:41]
	v_mfma_f32_16x16x32_bf16 v[38:41], v[26:29], v[106:109], v[102:105]
	v_mfma_f32_16x16x32_bf16 v[102:105], v[34:37], v[114:117], v[38:41]
	v_mfma_f32_16x16x32_bf16 v[38:41], v[46:49], v[106:109], v[90:93]
	v_mfma_f32_16x16x32_bf16 v[90:93], v[50:53], v[114:117], v[38:41]
	v_mfma_f32_16x16x32_bf16 v[38:41], v[26:29], v[138:141], v[70:73]
	v_mfma_f32_16x16x32_bf16 v[70:73], v[34:37], v[142:145], v[38:41]
	v_mfma_f32_16x16x32_bf16 v[38:41], v[46:49], v[138:141], v[58:61]
	v_mfma_f32_16x16x32_bf16 v[4:7], v[26:29], v[172:175], v[6:9]
	v_mfma_f32_16x16x32_bf16 v[58:61], v[50:53], v[142:145], v[38:41]
	v_mfma_f32_16x16x32_bf16 v[38:41], v[34:37], v[176:179], v[4:7]
	v_mfma_f32_16x16x32_bf16 v[4:7], v[46:49], v[172:175], v[14:17]
	v_mfma_f32_16x16x32_bf16 v[26:29], v[50:53], v[176:179], v[4:7]
	v_mfma_f32_16x16x32_bf16 v[4:7], v[62:65], v[86:89], v[18:21]
	v_mfma_f32_16x16x32_bf16 v[118:121], v[78:81], v[98:101], v[4:7]
	v_mfma_f32_16x16x32_bf16 v[4:7], v[82:85], v[86:89], v[30:33]
	v_mfma_f32_16x16x32_bf16 v[110:113], v[94:97], v[98:101], v[4:7]
	v_mfma_f32_16x16x32_bf16 v[4:7], v[62:65], v[106:109], v[66:69]
	v_mfma_f32_16x16x32_bf16 v[86:89], v[78:81], v[114:117], v[4:7]
	v_mfma_f32_16x16x32_bf16 v[4:7], v[82:85], v[106:109], v[74:77]
	v_mfma_f32_16x16x32_bf16 v[74:77], v[94:97], v[114:117], v[4:7]
	v_mfma_f32_16x16x32_bf16 v[4:7], v[62:65], v[138:141], v[54:57]
	v_mfma_f32_16x16x32_bf16 v[54:57], v[78:81], v[142:145], v[4:7]
	v_mfma_f32_16x16x32_bf16 v[4:7], v[82:85], v[138:141], v[42:45]
	v_mfma_f32_16x16x32_bf16 v[42:45], v[94:97], v[142:145], v[4:7]
	v_mfma_f32_16x16x32_bf16 v[4:7], v[62:65], v[172:175], v[22:25]
	v_mfma_f32_16x16x32_bf16 v[22:25], v[78:81], v[176:179], v[4:7]
	v_mfma_f32_16x16x32_bf16 v[4:7], v[82:85], v[172:175], v[10:13]
	v_mfma_f32_16x16x32_bf16 v[10:13], v[94:97], v[176:179], v[4:7]
	s_barrier
	s_mov_b32 m0, s73
	s_add_i32 s15, s14, 0x80
	buffer_load_dwordx4 v151, s[16:19], s15 offen lds
	s_mov_b32 m0, s74
	s_add_i32 s14, s14, 0x80080
	buffer_load_dwordx4 v158, s[16:19], s15 offen lds
	s_mov_b32 m0, s77
	s_bitset1_b32 s86, 7
	buffer_load_dwordx4 v151, s[16:19], s14 offen lds
	s_mov_b32 m0, s78
	s_nop 0
	buffer_load_dwordx4 v158, s[16:19], s14 offen lds
	s_mov_b32 m0, s75
	s_nop 0
	buffer_load_dwordx4 v3, s[8:11], s86 offen lds
	s_mov_b32 m0, s76
	s_nop 0
	buffer_load_dwordx4 v2, s[8:11], s86 offen lds
	s_waitcnt vmcnt(8)
	s_waitcnt lgkmcnt(0)
	s_barrier
	s_barrier
	s_add_i32 s39, s39, 2
	s_cmp_lt_u32 s39, 30
	s_mov_b64 s[18:19], s[42:43]
	s_cbranch_scc0 .LBB0_1241

.LBB0_1246:
	ds_read_b128 v[142:145], v247
	ds_read_b128 v[172:175], v247 offset:1024
	ds_read_b128 v[176:179], v247 offset:2048
	ds_read_b128 v[180:183], v247 offset:3072
	ds_read_b128 v[184:187], v248
	ds_read_b128 v[188:191], v248 offset:1024
	ds_read_b128 v[196:199], v248 offset:2048
	ds_read_b128 v[200:203], v248 offset:3072
	ds_read_b128 v[204:207], v156
	ds_read_b128 v[208:211], v156 offset:1024
	ds_read_b128 v[212:215], v156 offset:2048
	ds_read_b128 v[216:219], v156 offset:3072
	ds_read_b128 v[220:223], v156 offset:4096
	ds_read_b128 v[224:227], v156 offset:5120
	ds_read_b128 v[228:231], v156 offset:6144
	ds_read_b128 v[232:235], v156 offset:7168
	s_add_u32 s38, s18, 0x100
	s_addc_u32 s39, s19, 0
	s_add_i32 s85, s29, s18
	s_and_b64 s[14:15], s[42:43], exec
	s_cselect_b32 s45, 0, s38
	s_add_i32 s14, s18, 0x80
	s_mov_b32 m0, s79
	s_nop 0
	buffer_load_dwordx4 v132, s[8:11], s14 offen lds
	s_mov_b32 m0, s80
	s_nop 0
	buffer_load_dwordx4 v134, s[8:11], s14 offen lds
	s_waitcnt vmcnt(8)
	s_waitcnt lgkmcnt(0)
	s_barrier
	v_mfma_f32_16x16x32_bf16 v[126:129], v[142:145], v[204:207], v[126:129]
	v_mfma_f32_16x16x32_bf16 v[122:125], v[176:179], v[204:207], v[122:125]
	v_mfma_f32_16x16x32_bf16 v[102:105], v[142:145], v[212:215], v[102:105]
	v_mfma_f32_16x16x32_bf16 v[90:93], v[176:179], v[212:215], v[90:93]
	v_mfma_f32_16x16x32_bf16 v[70:73], v[142:145], v[220:223], v[70:73]
	v_mfma_f32_16x16x32_bf16 v[58:61], v[176:179], v[220:223], v[58:61]
	v_mfma_f32_16x16x32_bf16 v[38:41], v[142:145], v[228:231], v[38:41]
	v_mfma_f32_16x16x32_bf16 v[26:29], v[176:179], v[228:231], v[26:29]
	v_mfma_f32_16x16x32_bf16 v[118:121], v[184:187], v[204:207], v[118:121]
	v_mfma_f32_16x16x32_bf16 v[110:113], v[196:199], v[204:207], v[110:113]
	v_mfma_f32_16x16x32_bf16 v[86:89], v[184:187], v[212:215], v[86:89]
	v_mfma_f32_16x16x32_bf16 v[74:77], v[196:199], v[212:215], v[74:77]
	v_mfma_f32_16x16x32_bf16 v[54:57], v[184:187], v[220:223], v[54:57]
	v_mfma_f32_16x16x32_bf16 v[42:45], v[196:199], v[220:223], v[42:45]
	v_mfma_f32_16x16x32_bf16 v[22:25], v[184:187], v[228:231], v[22:25]
	v_mfma_f32_16x16x32_bf16 v[10:13], v[196:199], v[228:231], v[10:13]
	v_mfma_f32_16x16x32_bf16 v[126:129], v[172:175], v[208:211], v[126:129]
	v_mfma_f32_16x16x32_bf16 v[122:125], v[180:183], v[208:211], v[122:125]
	v_mfma_f32_16x16x32_bf16 v[102:105], v[172:175], v[216:219], v[102:105]
	v_mfma_f32_16x16x32_bf16 v[90:93], v[180:183], v[216:219], v[90:93]
	v_mfma_f32_16x16x32_bf16 v[70:73], v[172:175], v[224:227], v[70:73]
	v_mfma_f32_16x16x32_bf16 v[58:61], v[180:183], v[224:227], v[58:61]
	v_mfma_f32_16x16x32_bf16 v[38:41], v[172:175], v[232:235], v[38:41]
	v_mfma_f32_16x16x32_bf16 v[26:29], v[180:183], v[232:235], v[26:29]
	v_mfma_f32_16x16x32_bf16 v[118:121], v[188:191], v[208:211], v[118:121]
	v_mfma_f32_16x16x32_bf16 v[110:113], v[200:203], v[208:211], v[110:113]
	v_mfma_f32_16x16x32_bf16 v[86:89], v[188:191], v[216:219], v[86:89]
	v_mfma_f32_16x16x32_bf16 v[74:77], v[200:203], v[216:219], v[74:77]
	v_mfma_f32_16x16x32_bf16 v[54:57], v[188:191], v[224:227], v[54:57]
	v_mfma_f32_16x16x32_bf16 v[42:45], v[200:203], v[224:227], v[42:45]
	v_mfma_f32_16x16x32_bf16 v[22:25], v[188:191], v[232:235], v[22:25]
	v_mfma_f32_16x16x32_bf16 v[10:13], v[200:203], v[232:235], v[10:13]
	s_barrier
	ds_read_b128 v[204:207], v156 offset:16384
	ds_read_b128 v[208:211], v156 offset:17408
	ds_read_b128 v[212:215], v156 offset:18432
	ds_read_b128 v[216:219], v156 offset:19456
	ds_read_b128 v[220:223], v156 offset:20480
	ds_read_b128 v[224:227], v156 offset:21504
	ds_read_b128 v[228:231], v156 offset:22528
	ds_read_b128 v[232:235], v156 offset:23552
	s_and_b64 s[14:15], s[42:43], exec
	s_cselect_b32 s14, s5, s85
	s_mov_b32 m0, s66
	s_mov_b32 s18, s10
	s_mov_b32 s19, s11
	s_sub_i32 s14, s14, s16
	buffer_load_dwordx4 v151, s[16:19], s14 offen lds
	s_mov_b32 m0, s67
	s_add_i32 s15, s14, 0x80000
	buffer_load_dwordx4 v158, s[16:19], s14 offen lds
	s_mov_b32 m0, s68
	s_nop 0
	buffer_load_dwordx4 v151, s[16:19], s15 offen lds
	s_mov_b32 m0, s69
	s_nop 0
	buffer_load_dwordx4 v158, s[16:19], s15 offen lds
	s_mov_b32 m0, s65
	s_nop 0
	buffer_load_dwordx4 v138, s[8:11], s45 offen lds
	s_mov_b32 m0, s70
	s_nop 0
	buffer_load_dwordx4 v137, s[8:11], s45 offen lds
	s_waitcnt vmcnt(8)
	s_waitcnt lgkmcnt(0)
	s_barrier
	v_mfma_f32_16x16x32_bf16 v[114:117], v[142:145], v[204:207], v[114:117]
	v_mfma_f32_16x16x32_bf16 v[98:101], v[176:179], v[204:207], v[98:101]
	v_mfma_f32_16x16x32_bf16 v[82:85], v[142:145], v[212:215], v[82:85]
	v_mfma_f32_16x16x32_bf16 v[66:69], v[176:179], v[212:215], v[66:69]
	v_mfma_f32_16x16x32_bf16 v[50:53], v[142:145], v[220:223], v[50:53]
	v_mfma_f32_16x16x32_bf16 v[34:37], v[176:179], v[220:223], v[34:37]
	v_mfma_f32_16x16x32_bf16 v[18:21], v[142:145], v[228:231], v[18:21]
	v_mfma_f32_16x16x32_bf16 v[6:9], v[176:179], v[228:231], v[6:9]
	v_mfma_f32_16x16x32_bf16 v[106:109], v[184:187], v[204:207], v[106:109]
	v_mfma_f32_16x16x32_bf16 v[94:97], v[196:199], v[204:207], v[94:97]
	v_mfma_f32_16x16x32_bf16 v[78:81], v[184:187], v[212:215], v[78:81]
	v_mfma_f32_16x16x32_bf16 v[62:65], v[196:199], v[212:215], v[62:65]
	v_mfma_f32_16x16x32_bf16 v[46:49], v[184:187], v[220:223], v[46:49]
	v_mfma_f32_16x16x32_bf16 v[30:33], v[196:199], v[220:223], v[30:33]
	v_mfma_f32_16x16x32_bf16 v[14:17], v[184:187], v[228:231], v[14:17]
	v_mfma_f32_16x16x32_bf16 v[2:5], v[196:199], v[228:231], v[2:5]
	v_mfma_f32_16x16x32_bf16 v[114:117], v[172:175], v[208:211], v[114:117]
	v_mfma_f32_16x16x32_bf16 v[98:101], v[180:183], v[208:211], v[98:101]
	v_mfma_f32_16x16x32_bf16 v[82:85], v[172:175], v[216:219], v[82:85]
	v_mfma_f32_16x16x32_bf16 v[66:69], v[180:183], v[216:219], v[66:69]
	v_mfma_f32_16x16x32_bf16 v[50:53], v[172:175], v[224:227], v[50:53]
	v_mfma_f32_16x16x32_bf16 v[34:37], v[180:183], v[224:227], v[34:37]
	v_mfma_f32_16x16x32_bf16 v[18:21], v[172:175], v[232:235], v[18:21]
	v_mfma_f32_16x16x32_bf16 v[6:9], v[180:183], v[232:235], v[6:9]
	v_mfma_f32_16x16x32_bf16 v[106:109], v[188:191], v[208:211], v[106:109]
	v_mfma_f32_16x16x32_bf16 v[94:97], v[200:203], v[208:211], v[94:97]
	v_mfma_f32_16x16x32_bf16 v[78:81], v[188:191], v[216:219], v[78:81]
	v_mfma_f32_16x16x32_bf16 v[62:65], v[200:203], v[216:219], v[62:65]
	v_mfma_f32_16x16x32_bf16 v[46:49], v[188:191], v[224:227], v[46:49]
	v_mfma_f32_16x16x32_bf16 v[30:33], v[200:203], v[224:227], v[30:33]
	v_mfma_f32_16x16x32_bf16 v[14:17], v[188:191], v[232:235], v[14:17]
	v_mfma_f32_16x16x32_bf16 v[2:5], v[200:203], v[232:235], v[2:5]
	s_barrier
	ds_read_b128 v[142:145], v249
	ds_read_b128 v[172:175], v249 offset:1024
	ds_read_b128 v[176:179], v249 offset:2048
	ds_read_b128 v[180:183], v249 offset:3072
	ds_read_b128 v[184:187], v250
	ds_read_b128 v[188:191], v250 offset:1024
	ds_read_b128 v[196:199], v250 offset:2048
	ds_read_b128 v[200:203], v250 offset:3072
	ds_read_b128 v[204:207], v156 offset:32768
	ds_read_b128 v[208:211], v156 offset:33792
	ds_read_b128 v[212:215], v156 offset:34816
	ds_read_b128 v[216:219], v156 offset:35840
	ds_read_b128 v[220:223], v156 offset:36864
	ds_read_b128 v[224:227], v156 offset:37888
	ds_read_b128 v[228:231], v156 offset:38912
	ds_read_b128 v[232:235], v156 offset:39936
	s_mov_b32 m0, s71
	s_nop 0
	buffer_load_dwordx4 v140, s[8:11], s45 offen lds
	s_mov_b32 m0, s72
	s_nop 0
	buffer_load_dwordx4 v139, s[8:11], s45 offen lds
	s_waitcnt vmcnt(8)
	s_waitcnt lgkmcnt(0)
	s_barrier
	v_mfma_f32_16x16x32_bf16 v[126:129], v[142:145], v[204:207], v[126:129]
	v_mfma_f32_16x16x32_bf16 v[122:125], v[176:179], v[204:207], v[122:125]
	v_mfma_f32_16x16x32_bf16 v[102:105], v[142:145], v[212:215], v[102:105]
	v_mfma_f32_16x16x32_bf16 v[90:93], v[176:179], v[212:215], v[90:93]
	v_mfma_f32_16x16x32_bf16 v[70:73], v[142:145], v[220:223], v[70:73]
	v_mfma_f32_16x16x32_bf16 v[58:61], v[176:179], v[220:223], v[58:61]
	v_mfma_f32_16x16x32_bf16 v[38:41], v[142:145], v[228:231], v[38:41]
	v_mfma_f32_16x16x32_bf16 v[26:29], v[176:179], v[228:231], v[26:29]
	v_mfma_f32_16x16x32_bf16 v[118:121], v[184:187], v[204:207], v[118:121]
	v_mfma_f32_16x16x32_bf16 v[110:113], v[196:199], v[204:207], v[110:113]
	v_mfma_f32_16x16x32_bf16 v[86:89], v[184:187], v[212:215], v[86:89]
	v_mfma_f32_16x16x32_bf16 v[74:77], v[196:199], v[212:215], v[74:77]
	v_mfma_f32_16x16x32_bf16 v[54:57], v[184:187], v[220:223], v[54:57]
	v_mfma_f32_16x16x32_bf16 v[42:45], v[196:199], v[220:223], v[42:45]
	v_mfma_f32_16x16x32_bf16 v[22:25], v[184:187], v[228:231], v[22:25]
	v_mfma_f32_16x16x32_bf16 v[10:13], v[196:199], v[228:231], v[10:13]
	v_mfma_f32_16x16x32_bf16 v[126:129], v[172:175], v[208:211], v[126:129]
	v_mfma_f32_16x16x32_bf16 v[122:125], v[180:183], v[208:211], v[122:125]
	v_mfma_f32_16x16x32_bf16 v[102:105], v[172:175], v[216:219], v[102:105]
	v_mfma_f32_16x16x32_bf16 v[90:93], v[180:183], v[216:219], v[90:93]
	v_mfma_f32_16x16x32_bf16 v[70:73], v[172:175], v[224:227], v[70:73]
	v_mfma_f32_16x16x32_bf16 v[58:61], v[180:183], v[224:227], v[58:61]
	v_mfma_f32_16x16x32_bf16 v[38:41], v[172:175], v[232:235], v[38:41]
	v_mfma_f32_16x16x32_bf16 v[26:29], v[180:183], v[232:235], v[26:29]
	v_mfma_f32_16x16x32_bf16 v[118:121], v[188:191], v[208:211], v[118:121]
	v_mfma_f32_16x16x32_bf16 v[110:113], v[200:203], v[208:211], v[110:113]
	v_mfma_f32_16x16x32_bf16 v[86:89], v[188:191], v[216:219], v[86:89]
	v_mfma_f32_16x16x32_bf16 v[74:77], v[200:203], v[216:219], v[74:77]
	v_mfma_f32_16x16x32_bf16 v[54:57], v[188:191], v[224:227], v[54:57]
	v_mfma_f32_16x16x32_bf16 v[42:45], v[200:203], v[224:227], v[42:45]
	v_mfma_f32_16x16x32_bf16 v[22:25], v[188:191], v[232:235], v[22:25]
	v_mfma_f32_16x16x32_bf16 v[10:13], v[200:203], v[232:235], v[10:13]
	s_barrier
	ds_read_b128 v[204:207], v156 offset:49152
	ds_read_b128 v[208:211], v156 offset:50176
	ds_read_b128 v[212:215], v156 offset:51200
	ds_read_b128 v[216:219], v156 offset:52224
	ds_read_b128 v[220:223], v156 offset:53248
	ds_read_b128 v[224:227], v156 offset:54272
	ds_read_b128 v[228:231], v156 offset:55296
	ds_read_b128 v[232:235], v156 offset:56320
	s_mov_b32 m0, s73
	s_add_i32 s15, s14, 0x80
	buffer_load_dwordx4 v151, s[16:19], s15 offen lds
	s_mov_b32 m0, s74
	s_add_i32 s14, s14, 0x80080
	buffer_load_dwordx4 v158, s[16:19], s15 offen lds
	s_mov_b32 m0, s77
	s_bitset1_b32 s45, 7
	buffer_load_dwordx4 v151, s[16:19], s14 offen lds
	s_mov_b32 m0, s78
	s_nop 0
	buffer_load_dwordx4 v158, s[16:19], s14 offen lds
	s_mov_b32 m0, s75
	s_nop 0
	buffer_load_dwordx4 v138, s[8:11], s45 offen lds
	s_mov_b32 m0, s76
	s_nop 0
	buffer_load_dwordx4 v137, s[8:11], s45 offen lds
	s_waitcnt vmcnt(8)
	s_waitcnt lgkmcnt(0)
	s_barrier
	v_mfma_f32_16x16x32_bf16 v[114:117], v[142:145], v[204:207], v[114:117]
	v_mfma_f32_16x16x32_bf16 v[98:101], v[176:179], v[204:207], v[98:101]
	v_mfma_f32_16x16x32_bf16 v[82:85], v[142:145], v[212:215], v[82:85]
	v_mfma_f32_16x16x32_bf16 v[66:69], v[176:179], v[212:215], v[66:69]
	v_mfma_f32_16x16x32_bf16 v[50:53], v[142:145], v[220:223], v[50:53]
	v_mfma_f32_16x16x32_bf16 v[34:37], v[176:179], v[220:223], v[34:37]
	v_mfma_f32_16x16x32_bf16 v[18:21], v[142:145], v[228:231], v[18:21]
	v_mfma_f32_16x16x32_bf16 v[6:9], v[176:179], v[228:231], v[6:9]
	v_mfma_f32_16x16x32_bf16 v[106:109], v[184:187], v[204:207], v[106:109]
	v_mfma_f32_16x16x32_bf16 v[94:97], v[196:199], v[204:207], v[94:97]
	v_mfma_f32_16x16x32_bf16 v[78:81], v[184:187], v[212:215], v[78:81]
	v_mfma_f32_16x16x32_bf16 v[62:65], v[196:199], v[212:215], v[62:65]
	v_mfma_f32_16x16x32_bf16 v[46:49], v[184:187], v[220:223], v[46:49]
	v_mfma_f32_16x16x32_bf16 v[30:33], v[196:199], v[220:223], v[30:33]
	v_mfma_f32_16x16x32_bf16 v[14:17], v[184:187], v[228:231], v[14:17]
	v_mfma_f32_16x16x32_bf16 v[2:5], v[196:199], v[228:231], v[2:5]
	v_mfma_f32_16x16x32_bf16 v[114:117], v[172:175], v[208:211], v[114:117]
	v_mfma_f32_16x16x32_bf16 v[98:101], v[180:183], v[208:211], v[98:101]
	v_mfma_f32_16x16x32_bf16 v[82:85], v[172:175], v[216:219], v[82:85]
	v_mfma_f32_16x16x32_bf16 v[66:69], v[180:183], v[216:219], v[66:69]
	v_mfma_f32_16x16x32_bf16 v[50:53], v[172:175], v[224:227], v[50:53]
	v_mfma_f32_16x16x32_bf16 v[34:37], v[180:183], v[224:227], v[34:37]
	v_mfma_f32_16x16x32_bf16 v[18:21], v[172:175], v[232:235], v[18:21]
	v_mfma_f32_16x16x32_bf16 v[6:9], v[180:183], v[232:235], v[6:9]
	v_mfma_f32_16x16x32_bf16 v[106:109], v[188:191], v[208:211], v[106:109]
	v_mfma_f32_16x16x32_bf16 v[94:97], v[200:203], v[208:211], v[94:97]
	v_mfma_f32_16x16x32_bf16 v[78:81], v[188:191], v[216:219], v[78:81]
	v_mfma_f32_16x16x32_bf16 v[62:65], v[200:203], v[216:219], v[62:65]
	v_mfma_f32_16x16x32_bf16 v[46:49], v[188:191], v[224:227], v[46:49]
	v_mfma_f32_16x16x32_bf16 v[30:33], v[200:203], v[224:227], v[30:33]
	v_mfma_f32_16x16x32_bf16 v[14:17], v[188:191], v[232:235], v[14:17]
	v_mfma_f32_16x16x32_bf16 v[2:5], v[200:203], v[232:235], v[2:5]
	s_barrier
	s_add_i32 s44, s44, 2
	s_cmp_gt_u32 s44, 29
	s_cbranch_scc1 .LBB0_1248
	s_mov_b64 s[18:19], s[38:39]
	s_branch .LBB0_1244

.LBB0_1456:
	ds_read_b128 v[66:69], v159
	ds_read_b128 v[70:73], v159 offset:1024
	ds_read_b128 v[74:77], v159 offset:2048
	ds_read_b128 v[78:81], v159 offset:3072
	ds_read_b128 v[82:85], v160
	ds_read_b128 v[86:89], v160 offset:1024
	ds_read_b128 v[90:93], v160 offset:2048
	ds_read_b128 v[94:97], v160 offset:3072
	ds_read_b128 v[98:101], v161
	ds_read_b128 v[102:105], v161 offset:1024
	ds_read_b128 v[106:109], v161 offset:2048
	ds_read_b128 v[110:113], v161 offset:3072
	ds_read_b128 v[114:117], v161 offset:4096
	ds_read_b128 v[118:121], v161 offset:5120
	ds_read_b128 v[122:125], v161 offset:6144
	ds_read_b128 v[126:129], v161 offset:7168
	s_add_i32 s10, s44, s48
	s_sub_i32 s10, s10, s4
	s_add_i32 s47, s46, s48
	s_add_i32 s10, s10, 0x7ff80
	s_cmp_eq_u32 s45, 28
	s_cselect_b32 s50, 0, s48
	s_mov_b32 m0, s67
	s_nop 0
	buffer_load_dwordx4 v1, s[4:7], s10 offen lds
	s_mov_b32 m0, s68
	s_nop 0
	buffer_load_dwordx4 v153, s[4:7], s10 offen lds
	s_waitcnt vmcnt(8)
	s_waitcnt lgkmcnt(0)
	s_barrier
	v_mfma_f32_16x16x32_bf16 v[62:65], v[66:69], v[98:101], v[62:65]
	v_mfma_f32_16x16x32_bf16 v[58:61], v[74:77], v[98:101], v[58:61]
	v_mfma_f32_16x16x32_bf16 v[54:57], v[66:69], v[106:109], v[54:57]
	v_mfma_f32_16x16x32_bf16 v[50:53], v[74:77], v[106:109], v[50:53]
	v_mfma_f32_16x16x32_bf16 v[38:41], v[66:69], v[114:117], v[38:41]
	v_mfma_f32_16x16x32_bf16 v[34:37], v[74:77], v[114:117], v[34:37]
	v_mfma_f32_16x16x32_bf16 v[22:25], v[66:69], v[122:125], v[22:25]
	v_mfma_f32_16x16x32_bf16 v[18:21], v[74:77], v[122:125], v[18:21]
	v_mfma_f32_16x16x32_bf16 v[46:49], v[82:85], v[98:101], v[46:49]
	v_mfma_f32_16x16x32_bf16 v[42:45], v[90:93], v[98:101], v[42:45]
	v_mfma_f32_16x16x32_bf16 v[30:33], v[82:85], v[106:109], v[30:33]
	v_mfma_f32_16x16x32_bf16 v[26:29], v[90:93], v[106:109], v[26:29]
	v_mfma_f32_16x16x32_bf16 v[14:17], v[82:85], v[114:117], v[14:17]
	v_mfma_f32_16x16x32_bf16 v[10:13], v[90:93], v[114:117], v[10:13]
	v_mfma_f32_16x16x32_bf16 v[6:9], v[82:85], v[122:125], v[6:9]
	v_mfma_f32_16x16x32_bf16 v[2:5], v[90:93], v[122:125], v[2:5]
	v_mfma_f32_16x16x32_bf16 v[62:65], v[70:73], v[102:105], v[62:65]
	v_mfma_f32_16x16x32_bf16 v[58:61], v[78:81], v[102:105], v[58:61]
	v_mfma_f32_16x16x32_bf16 v[54:57], v[70:73], v[110:113], v[54:57]
	v_mfma_f32_16x16x32_bf16 v[50:53], v[78:81], v[110:113], v[50:53]
	v_mfma_f32_16x16x32_bf16 v[38:41], v[70:73], v[118:121], v[38:41]
	v_mfma_f32_16x16x32_bf16 v[34:37], v[78:81], v[118:121], v[34:37]
	v_mfma_f32_16x16x32_bf16 v[22:25], v[70:73], v[126:129], v[22:25]
	v_mfma_f32_16x16x32_bf16 v[18:21], v[78:81], v[126:129], v[18:21]
	v_mfma_f32_16x16x32_bf16 v[46:49], v[86:89], v[102:105], v[46:49]
	v_mfma_f32_16x16x32_bf16 v[42:45], v[94:97], v[102:105], v[42:45]
	v_mfma_f32_16x16x32_bf16 v[30:33], v[86:89], v[110:113], v[30:33]
	v_mfma_f32_16x16x32_bf16 v[26:29], v[94:97], v[110:113], v[26:29]
	v_mfma_f32_16x16x32_bf16 v[14:17], v[86:89], v[118:121], v[14:17]
	v_mfma_f32_16x16x32_bf16 v[10:13], v[94:97], v[118:121], v[10:13]
	v_mfma_f32_16x16x32_bf16 v[6:9], v[86:89], v[126:129], v[6:9]
	v_mfma_f32_16x16x32_bf16 v[2:5], v[94:97], v[126:129], v[2:5]
	s_barrier
	s_cselect_b32 s47, s31, s47
	s_mov_b32 m0, s53
	s_mov_b32 s10, s6
	s_mov_b32 s11, s7
	s_cselect_b32 s51, s27, s44
	s_sub_i32 s47, s47, s8
	buffer_load_dwordx4 v152, s[8:11], s47 offen lds
	s_mov_b32 m0, s54
	s_add_i32 s73, s47, 0x80000
	buffer_load_dwordx4 v154, s[8:11], s47 offen lds
	s_mov_b32 m0, s55
	s_add_i32 s51, s51, s50
	buffer_load_dwordx4 v152, s[8:11], s73 offen lds
	s_mov_b32 m0, s56
	s_sub_i32 s50, s51, s4
	buffer_load_dwordx4 v154, s[8:11], s73 offen lds
	s_mov_b32 m0, s43
	s_nop 0
	buffer_load_dwordx4 v1, s[4:7], s50 offen lds
	s_mov_b32 m0, s57
	s_nop 0
	buffer_load_dwordx4 v153, s[4:7], s50 offen lds
	s_waitcnt vmcnt(8)
	s_waitcnt lgkmcnt(0)
	s_barrier
	s_barrier
	ds_read_b128 v[66:69], v162
	ds_read_b128 v[70:73], v162 offset:1024
	ds_read_b128 v[74:77], v162 offset:2048
	ds_read_b128 v[78:81], v162 offset:3072
	ds_read_b128 v[82:85], v163
	ds_read_b128 v[86:89], v163 offset:1024
	ds_read_b128 v[90:93], v163 offset:2048
	ds_read_b128 v[94:97], v163 offset:3072
	ds_read_b128 v[98:101], v161 offset:32768
	ds_read_b128 v[102:105], v161 offset:33792
	ds_read_b128 v[106:109], v161 offset:34816
	ds_read_b128 v[110:113], v161 offset:35840
	ds_read_b128 v[114:117], v161 offset:36864
	ds_read_b128 v[118:121], v161 offset:37888
	ds_read_b128 v[122:125], v161 offset:38912
	ds_read_b128 v[126:129], v161 offset:39936
	s_add_i32 s51, s50, 0x80000
	s_mov_b32 m0, s58
	s_nop 0
	buffer_load_dwordx4 v1, s[4:7], s51 offen lds
	s_mov_b32 m0, s59
	s_nop 0
	buffer_load_dwordx4 v153, s[4:7], s51 offen lds
	s_waitcnt vmcnt(8)
	s_waitcnt lgkmcnt(0)
	s_barrier
	v_mfma_f32_16x16x32_bf16 v[62:65], v[66:69], v[98:101], v[62:65]
	v_mfma_f32_16x16x32_bf16 v[58:61], v[74:77], v[98:101], v[58:61]
	v_mfma_f32_16x16x32_bf16 v[54:57], v[66:69], v[106:109], v[54:57]
	v_mfma_f32_16x16x32_bf16 v[50:53], v[74:77], v[106:109], v[50:53]
	v_mfma_f32_16x16x32_bf16 v[38:41], v[66:69], v[114:117], v[38:41]
	v_mfma_f32_16x16x32_bf16 v[34:37], v[74:77], v[114:117], v[34:37]
	v_mfma_f32_16x16x32_bf16 v[22:25], v[66:69], v[122:125], v[22:25]
	v_mfma_f32_16x16x32_bf16 v[18:21], v[74:77], v[122:125], v[18:21]
	v_mfma_f32_16x16x32_bf16 v[46:49], v[82:85], v[98:101], v[46:49]
	v_mfma_f32_16x16x32_bf16 v[42:45], v[90:93], v[98:101], v[42:45]
	v_mfma_f32_16x16x32_bf16 v[30:33], v[82:85], v[106:109], v[30:33]
	v_mfma_f32_16x16x32_bf16 v[26:29], v[90:93], v[106:109], v[26:29]
	v_mfma_f32_16x16x32_bf16 v[14:17], v[82:85], v[114:117], v[14:17]
	v_mfma_f32_16x16x32_bf16 v[10:13], v[90:93], v[114:117], v[10:13]
	v_mfma_f32_16x16x32_bf16 v[6:9], v[82:85], v[122:125], v[6:9]
	v_mfma_f32_16x16x32_bf16 v[2:5], v[90:93], v[122:125], v[2:5]
	v_mfma_f32_16x16x32_bf16 v[62:65], v[70:73], v[102:105], v[62:65]
	v_mfma_f32_16x16x32_bf16 v[58:61], v[78:81], v[102:105], v[58:61]
	v_mfma_f32_16x16x32_bf16 v[54:57], v[70:73], v[110:113], v[54:57]
	v_mfma_f32_16x16x32_bf16 v[50:53], v[78:81], v[110:113], v[50:53]
	v_mfma_f32_16x16x32_bf16 v[38:41], v[70:73], v[118:121], v[38:41]
	v_mfma_f32_16x16x32_bf16 v[34:37], v[78:81], v[118:121], v[34:37]
	v_mfma_f32_16x16x32_bf16 v[22:25], v[70:73], v[126:129], v[22:25]
	v_mfma_f32_16x16x32_bf16 v[18:21], v[78:81], v[126:129], v[18:21]
	v_mfma_f32_16x16x32_bf16 v[46:49], v[86:89], v[102:105], v[46:49]
	v_mfma_f32_16x16x32_bf16 v[42:45], v[94:97], v[102:105], v[42:45]
	v_mfma_f32_16x16x32_bf16 v[30:33], v[86:89], v[110:113], v[30:33]
	v_mfma_f32_16x16x32_bf16 v[26:29], v[94:97], v[110:113], v[26:29]
	v_mfma_f32_16x16x32_bf16 v[14:17], v[86:89], v[118:121], v[14:17]
	v_mfma_f32_16x16x32_bf16 v[10:13], v[94:97], v[118:121], v[10:13]
	v_mfma_f32_16x16x32_bf16 v[6:9], v[86:89], v[126:129], v[6:9]
	v_mfma_f32_16x16x32_bf16 v[2:5], v[94:97], v[126:129], v[2:5]
	s_barrier
	s_mov_b32 m0, s61
	s_add_i32 s51, s47, 0x80
	buffer_load_dwordx4 v152, s[8:11], s51 offen lds
	s_mov_b32 m0, s62
	s_add_i32 s47, s47, 0x80080
	buffer_load_dwordx4 v154, s[8:11], s51 offen lds
	s_mov_b32 m0, s65
	s_addk_i32 s50, 0x80
	buffer_load_dwordx4 v152, s[8:11], s47 offen lds
	s_mov_b32 m0, s66
	s_nop 0
	buffer_load_dwordx4 v154, s[8:11], s47 offen lds
	s_mov_b32 m0, s63
	s_nop 0
	buffer_load_dwordx4 v1, s[4:7], s50 offen lds
	s_mov_b32 m0, s64
	s_nop 0
	buffer_load_dwordx4 v153, s[4:7], s50 offen lds
	s_waitcnt vmcnt(8)
	s_waitcnt lgkmcnt(0)
	s_barrier
	s_barrier
	s_add_i32 s45, s45, 2
	s_add_u32 s48, s48, 0x100
	s_addc_u32 s49, s49, 0
	s_cmp_lt_u32 s45, 30
	s_cbranch_scc1 .LBB0_1456
	s_mov_b64 s[10:11], 0

.LBB0_1460:
	ds_read_b128 v[132:135], v159
	ds_read_b128 v[136:139], v159 offset:1024
	ds_read_b128 v[140:143], v159 offset:2048
	ds_read_b128 v[164:167], v159 offset:3072
	ds_read_b128 v[168:171], v160
	ds_read_b128 v[172:175], v160 offset:1024
	ds_read_b128 v[176:179], v160 offset:2048
	ds_read_b128 v[180:183], v160 offset:3072
	ds_read_b128 v[184:187], v161
	ds_read_b128 v[188:191], v161 offset:1024
	ds_read_b128 v[196:199], v161 offset:2048
	ds_read_b128 v[200:203], v161 offset:3072
	ds_read_b128 v[204:207], v161 offset:4096
	ds_read_b128 v[208:211], v161 offset:5120
	ds_read_b128 v[212:215], v161 offset:6144
	ds_read_b128 v[216:219], v161 offset:7168
	s_add_i32 s10, s44, s48
	s_sub_i32 s10, s10, s4
	s_add_i32 s47, s46, s48
	s_add_i32 s10, s10, 0x7ff80
	s_cmp_eq_u32 s45, 28
	s_cselect_b32 s50, 0, s48
	s_mov_b32 m0, s67
	s_nop 0
	buffer_load_dwordx4 v1, s[4:7], s10 offen lds
	s_mov_b32 m0, s68
	s_nop 0
	buffer_load_dwordx4 v153, s[4:7], s10 offen lds
	s_waitcnt vmcnt(8)
	s_waitcnt lgkmcnt(0)
	s_barrier
	v_mfma_f32_16x16x32_bf16 v[62:65], v[132:135], v[184:187], v[62:65]
	v_mfma_f32_16x16x32_bf16 v[58:61], v[140:143], v[184:187], v[58:61]
	v_mfma_f32_16x16x32_bf16 v[54:57], v[132:135], v[196:199], v[54:57]
	v_mfma_f32_16x16x32_bf16 v[50:53], v[140:143], v[196:199], v[50:53]
	v_mfma_f32_16x16x32_bf16 v[38:41], v[132:135], v[204:207], v[38:41]
	v_mfma_f32_16x16x32_bf16 v[34:37], v[140:143], v[204:207], v[34:37]
	v_mfma_f32_16x16x32_bf16 v[22:25], v[132:135], v[212:215], v[22:25]
	v_mfma_f32_16x16x32_bf16 v[18:21], v[140:143], v[212:215], v[18:21]
	v_mfma_f32_16x16x32_bf16 v[46:49], v[168:171], v[184:187], v[46:49]
	v_mfma_f32_16x16x32_bf16 v[42:45], v[176:179], v[184:187], v[42:45]
	v_mfma_f32_16x16x32_bf16 v[30:33], v[168:171], v[196:199], v[30:33]
	v_mfma_f32_16x16x32_bf16 v[26:29], v[176:179], v[196:199], v[26:29]
	v_mfma_f32_16x16x32_bf16 v[14:17], v[168:171], v[204:207], v[14:17]
	v_mfma_f32_16x16x32_bf16 v[10:13], v[176:179], v[204:207], v[10:13]
	v_mfma_f32_16x16x32_bf16 v[6:9], v[168:171], v[212:215], v[6:9]
	v_mfma_f32_16x16x32_bf16 v[2:5], v[176:179], v[212:215], v[2:5]
	v_mfma_f32_16x16x32_bf16 v[62:65], v[136:139], v[188:191], v[62:65]
	v_mfma_f32_16x16x32_bf16 v[58:61], v[164:167], v[188:191], v[58:61]
	v_mfma_f32_16x16x32_bf16 v[54:57], v[136:139], v[200:203], v[54:57]
	v_mfma_f32_16x16x32_bf16 v[50:53], v[164:167], v[200:203], v[50:53]
	v_mfma_f32_16x16x32_bf16 v[38:41], v[136:139], v[208:211], v[38:41]
	v_mfma_f32_16x16x32_bf16 v[34:37], v[164:167], v[208:211], v[34:37]
	v_mfma_f32_16x16x32_bf16 v[22:25], v[136:139], v[216:219], v[22:25]
	v_mfma_f32_16x16x32_bf16 v[18:21], v[164:167], v[216:219], v[18:21]
	v_mfma_f32_16x16x32_bf16 v[46:49], v[172:175], v[188:191], v[46:49]
	v_mfma_f32_16x16x32_bf16 v[42:45], v[180:183], v[188:191], v[42:45]
	v_mfma_f32_16x16x32_bf16 v[30:33], v[172:175], v[200:203], v[30:33]
	v_mfma_f32_16x16x32_bf16 v[26:29], v[180:183], v[200:203], v[26:29]
	v_mfma_f32_16x16x32_bf16 v[14:17], v[172:175], v[208:211], v[14:17]
	v_mfma_f32_16x16x32_bf16 v[10:13], v[180:183], v[208:211], v[10:13]
	v_mfma_f32_16x16x32_bf16 v[6:9], v[172:175], v[216:219], v[6:9]
	v_mfma_f32_16x16x32_bf16 v[2:5], v[180:183], v[216:219], v[2:5]
	s_barrier
	ds_read_b128 v[184:187], v161 offset:16384
	ds_read_b128 v[188:191], v161 offset:17408
	ds_read_b128 v[196:199], v161 offset:18432
	ds_read_b128 v[200:203], v161 offset:19456
	ds_read_b128 v[204:207], v161 offset:20480
	ds_read_b128 v[208:211], v161 offset:21504
	ds_read_b128 v[212:215], v161 offset:22528
	ds_read_b128 v[216:219], v161 offset:23552
	s_cselect_b32 s47, s31, s47
	s_mov_b32 m0, s53
	s_mov_b32 s10, s6
	s_mov_b32 s11, s7
	s_cselect_b32 s51, s27, s44
	s_sub_i32 s47, s47, s8
	buffer_load_dwordx4 v152, s[8:11], s47 offen lds
	s_mov_b32 m0, s54
	s_add_i32 s73, s47, 0x80000
	buffer_load_dwordx4 v154, s[8:11], s47 offen lds
	s_mov_b32 m0, s55
	s_add_i32 s51, s51, s50
	buffer_load_dwordx4 v152, s[8:11], s73 offen lds
	s_mov_b32 m0, s56
	s_sub_i32 s50, s51, s4
	buffer_load_dwordx4 v154, s[8:11], s73 offen lds
	s_mov_b32 m0, s43
	s_nop 0
	buffer_load_dwordx4 v1, s[4:7], s50 offen lds
	s_mov_b32 m0, s57
	s_nop 0
	buffer_load_dwordx4 v153, s[4:7], s50 offen lds
	s_waitcnt vmcnt(8)
	s_waitcnt lgkmcnt(0)
	s_barrier
	v_mfma_f32_16x16x32_bf16 v[126:129], v[132:135], v[184:187], v[126:129]
	v_mfma_f32_16x16x32_bf16 v[122:125], v[140:143], v[184:187], v[122:125]
	v_mfma_f32_16x16x32_bf16 v[110:113], v[132:135], v[196:199], v[110:113]
	v_mfma_f32_16x16x32_bf16 v[106:109], v[140:143], v[196:199], v[106:109]
	v_mfma_f32_16x16x32_bf16 v[94:97], v[132:135], v[204:207], v[94:97]
	v_mfma_f32_16x16x32_bf16 v[90:93], v[140:143], v[204:207], v[90:93]
	v_mfma_f32_16x16x32_bf16 v[78:81], v[132:135], v[212:215], v[78:81]
	v_mfma_f32_16x16x32_bf16 v[74:77], v[140:143], v[212:215], v[74:77]
	v_mfma_f32_16x16x32_bf16 v[118:121], v[168:171], v[184:187], v[118:121]
	v_mfma_f32_16x16x32_bf16 v[114:117], v[176:179], v[184:187], v[114:117]
	v_mfma_f32_16x16x32_bf16 v[102:105], v[168:171], v[196:199], v[102:105]
	v_mfma_f32_16x16x32_bf16 v[98:101], v[176:179], v[196:199], v[98:101]
	v_mfma_f32_16x16x32_bf16 v[86:89], v[168:171], v[204:207], v[86:89]
	v_mfma_f32_16x16x32_bf16 v[82:85], v[176:179], v[204:207], v[82:85]
	v_mfma_f32_16x16x32_bf16 v[70:73], v[168:171], v[212:215], v[70:73]
	v_mfma_f32_16x16x32_bf16 v[66:69], v[176:179], v[212:215], v[66:69]
	v_mfma_f32_16x16x32_bf16 v[126:129], v[136:139], v[188:191], v[126:129]
	v_mfma_f32_16x16x32_bf16 v[122:125], v[164:167], v[188:191], v[122:125]
	v_mfma_f32_16x16x32_bf16 v[110:113], v[136:139], v[200:203], v[110:113]
	v_mfma_f32_16x16x32_bf16 v[106:109], v[164:167], v[200:203], v[106:109]
	v_mfma_f32_16x16x32_bf16 v[94:97], v[136:139], v[208:211], v[94:97]
	v_mfma_f32_16x16x32_bf16 v[90:93], v[164:167], v[208:211], v[90:93]
	v_mfma_f32_16x16x32_bf16 v[78:81], v[136:139], v[216:219], v[78:81]
	v_mfma_f32_16x16x32_bf16 v[74:77], v[164:167], v[216:219], v[74:77]
	v_mfma_f32_16x16x32_bf16 v[118:121], v[172:175], v[188:191], v[118:121]
	v_mfma_f32_16x16x32_bf16 v[114:117], v[180:183], v[188:191], v[114:117]
	v_mfma_f32_16x16x32_bf16 v[102:105], v[172:175], v[200:203], v[102:105]
	v_mfma_f32_16x16x32_bf16 v[98:101], v[180:183], v[200:203], v[98:101]
	v_mfma_f32_16x16x32_bf16 v[86:89], v[172:175], v[208:211], v[86:89]
	v_mfma_f32_16x16x32_bf16 v[82:85], v[180:183], v[208:211], v[82:85]
	v_mfma_f32_16x16x32_bf16 v[70:73], v[172:175], v[216:219], v[70:73]
	v_mfma_f32_16x16x32_bf16 v[66:69], v[180:183], v[216:219], v[66:69]
	s_barrier
	ds_read_b128 v[132:135], v162
	ds_read_b128 v[136:139], v162 offset:1024
	ds_read_b128 v[140:143], v162 offset:2048
	ds_read_b128 v[164:167], v162 offset:3072
	ds_read_b128 v[168:171], v163
	ds_read_b128 v[172:175], v163 offset:1024
	ds_read_b128 v[176:179], v163 offset:2048
	ds_read_b128 v[180:183], v163 offset:3072
	ds_read_b128 v[184:187], v161 offset:32768
	ds_read_b128 v[188:191], v161 offset:33792
	ds_read_b128 v[196:199], v161 offset:34816
	ds_read_b128 v[200:203], v161 offset:35840
	ds_read_b128 v[204:207], v161 offset:36864
	ds_read_b128 v[208:211], v161 offset:37888
	ds_read_b128 v[212:215], v161 offset:38912
	ds_read_b128 v[216:219], v161 offset:39936
	s_add_i32 s51, s50, 0x80000
	s_mov_b32 m0, s58
	s_nop 0
	buffer_load_dwordx4 v1, s[4:7], s51 offen lds
	s_mov_b32 m0, s59
	s_nop 0
	buffer_load_dwordx4 v153, s[4:7], s51 offen lds
	s_waitcnt vmcnt(8)
	s_waitcnt lgkmcnt(0)
	s_barrier
	v_mfma_f32_16x16x32_bf16 v[62:65], v[132:135], v[184:187], v[62:65]
	v_mfma_f32_16x16x32_bf16 v[58:61], v[140:143], v[184:187], v[58:61]
	v_mfma_f32_16x16x32_bf16 v[54:57], v[132:135], v[196:199], v[54:57]
	v_mfma_f32_16x16x32_bf16 v[50:53], v[140:143], v[196:199], v[50:53]
	v_mfma_f32_16x16x32_bf16 v[38:41], v[132:135], v[204:207], v[38:41]
	v_mfma_f32_16x16x32_bf16 v[34:37], v[140:143], v[204:207], v[34:37]
	v_mfma_f32_16x16x32_bf16 v[22:25], v[132:135], v[212:215], v[22:25]
	v_mfma_f32_16x16x32_bf16 v[18:21], v[140:143], v[212:215], v[18:21]
	v_mfma_f32_16x16x32_bf16 v[46:49], v[168:171], v[184:187], v[46:49]
	v_mfma_f32_16x16x32_bf16 v[42:45], v[176:179], v[184:187], v[42:45]
	v_mfma_f32_16x16x32_bf16 v[30:33], v[168:171], v[196:199], v[30:33]
	v_mfma_f32_16x16x32_bf16 v[26:29], v[176:179], v[196:199], v[26:29]
	v_mfma_f32_16x16x32_bf16 v[14:17], v[168:171], v[204:207], v[14:17]
	v_mfma_f32_16x16x32_bf16 v[10:13], v[176:179], v[204:207], v[10:13]
	v_mfma_f32_16x16x32_bf16 v[6:9], v[168:171], v[212:215], v[6:9]
	v_mfma_f32_16x16x32_bf16 v[2:5], v[176:179], v[212:215], v[2:5]
	v_mfma_f32_16x16x32_bf16 v[62:65], v[136:139], v[188:191], v[62:65]
	v_mfma_f32_16x16x32_bf16 v[58:61], v[164:167], v[188:191], v[58:61]
	v_mfma_f32_16x16x32_bf16 v[54:57], v[136:139], v[200:203], v[54:57]
	v_mfma_f32_16x16x32_bf16 v[50:53], v[164:167], v[200:203], v[50:53]
	v_mfma_f32_16x16x32_bf16 v[38:41], v[136:139], v[208:211], v[38:41]
	v_mfma_f32_16x16x32_bf16 v[34:37], v[164:167], v[208:211], v[34:37]
	v_mfma_f32_16x16x32_bf16 v[22:25], v[136:139], v[216:219], v[22:25]
	v_mfma_f32_16x16x32_bf16 v[18:21], v[164:167], v[216:219], v[18:21]
	v_mfma_f32_16x16x32_bf16 v[46:49], v[172:175], v[188:191], v[46:49]
	v_mfma_f32_16x16x32_bf16 v[42:45], v[180:183], v[188:191], v[42:45]
	v_mfma_f32_16x16x32_bf16 v[30:33], v[172:175], v[200:203], v[30:33]
	v_mfma_f32_16x16x32_bf16 v[26:29], v[180:183], v[200:203], v[26:29]
	v_mfma_f32_16x16x32_bf16 v[14:17], v[172:175], v[208:211], v[14:17]
	v_mfma_f32_16x16x32_bf16 v[10:13], v[180:183], v[208:211], v[10:13]
	v_mfma_f32_16x16x32_bf16 v[6:9], v[172:175], v[216:219], v[6:9]
	v_mfma_f32_16x16x32_bf16 v[2:5], v[180:183], v[216:219], v[2:5]
	s_barrier
	ds_read_b128 v[184:187], v161 offset:49152
	ds_read_b128 v[188:191], v161 offset:50176
	ds_read_b128 v[196:199], v161 offset:51200
	ds_read_b128 v[200:203], v161 offset:52224
	ds_read_b128 v[204:207], v161 offset:53248
	ds_read_b128 v[208:211], v161 offset:54272
	ds_read_b128 v[212:215], v161 offset:55296
	ds_read_b128 v[216:219], v161 offset:56320
	s_mov_b32 m0, s61
	s_add_i32 s51, s47, 0x80
	buffer_load_dwordx4 v152, s[8:11], s51 offen lds
	s_mov_b32 m0, s62
	s_add_i32 s47, s47, 0x80080
	buffer_load_dwordx4 v154, s[8:11], s51 offen lds
	s_mov_b32 m0, s65
	s_addk_i32 s50, 0x80
	buffer_load_dwordx4 v152, s[8:11], s47 offen lds
	s_mov_b32 m0, s66
	s_nop 0
	buffer_load_dwordx4 v154, s[8:11], s47 offen lds
	s_mov_b32 m0, s63
	s_nop 0
	buffer_load_dwordx4 v1, s[4:7], s50 offen lds
	s_mov_b32 m0, s64
	s_nop 0
	buffer_load_dwordx4 v153, s[4:7], s50 offen lds
	s_waitcnt vmcnt(8)
	s_waitcnt lgkmcnt(0)
	s_barrier
	v_mfma_f32_16x16x32_bf16 v[126:129], v[132:135], v[184:187], v[126:129]
	v_mfma_f32_16x16x32_bf16 v[122:125], v[140:143], v[184:187], v[122:125]
	v_mfma_f32_16x16x32_bf16 v[110:113], v[132:135], v[196:199], v[110:113]
	v_mfma_f32_16x16x32_bf16 v[106:109], v[140:143], v[196:199], v[106:109]
	v_mfma_f32_16x16x32_bf16 v[94:97], v[132:135], v[204:207], v[94:97]
	v_mfma_f32_16x16x32_bf16 v[90:93], v[140:143], v[204:207], v[90:93]
	v_mfma_f32_16x16x32_bf16 v[78:81], v[132:135], v[212:215], v[78:81]
	v_mfma_f32_16x16x32_bf16 v[74:77], v[140:143], v[212:215], v[74:77]
	v_mfma_f32_16x16x32_bf16 v[118:121], v[168:171], v[184:187], v[118:121]
	v_mfma_f32_16x16x32_bf16 v[114:117], v[176:179], v[184:187], v[114:117]
	v_mfma_f32_16x16x32_bf16 v[102:105], v[168:171], v[196:199], v[102:105]
	v_mfma_f32_16x16x32_bf16 v[98:101], v[176:179], v[196:199], v[98:101]
	v_mfma_f32_16x16x32_bf16 v[86:89], v[168:171], v[204:207], v[86:89]
	v_mfma_f32_16x16x32_bf16 v[82:85], v[176:179], v[204:207], v[82:85]
	v_mfma_f32_16x16x32_bf16 v[70:73], v[168:171], v[212:215], v[70:73]
	v_mfma_f32_16x16x32_bf16 v[66:69], v[176:179], v[212:215], v[66:69]
	v_mfma_f32_16x16x32_bf16 v[126:129], v[136:139], v[188:191], v[126:129]
	v_mfma_f32_16x16x32_bf16 v[122:125], v[164:167], v[188:191], v[122:125]
	v_mfma_f32_16x16x32_bf16 v[110:113], v[136:139], v[200:203], v[110:113]
	v_mfma_f32_16x16x32_bf16 v[106:109], v[164:167], v[200:203], v[106:109]
	v_mfma_f32_16x16x32_bf16 v[94:97], v[136:139], v[208:211], v[94:97]
	v_mfma_f32_16x16x32_bf16 v[90:93], v[164:167], v[208:211], v[90:93]
	v_mfma_f32_16x16x32_bf16 v[78:81], v[136:139], v[216:219], v[78:81]
	v_mfma_f32_16x16x32_bf16 v[74:77], v[164:167], v[216:219], v[74:77]
	v_mfma_f32_16x16x32_bf16 v[118:121], v[172:175], v[188:191], v[118:121]
	v_mfma_f32_16x16x32_bf16 v[114:117], v[180:183], v[188:191], v[114:117]
	v_mfma_f32_16x16x32_bf16 v[102:105], v[172:175], v[200:203], v[102:105]
	v_mfma_f32_16x16x32_bf16 v[98:101], v[180:183], v[200:203], v[98:101]
	v_mfma_f32_16x16x32_bf16 v[86:89], v[172:175], v[208:211], v[86:89]
	v_mfma_f32_16x16x32_bf16 v[82:85], v[180:183], v[208:211], v[82:85]
	v_mfma_f32_16x16x32_bf16 v[70:73], v[172:175], v[216:219], v[70:73]
	v_mfma_f32_16x16x32_bf16 v[66:69], v[180:183], v[216:219], v[66:69]
	s_barrier
	s_add_i32 s45, s45, 2
	s_add_u32 s48, s48, 0x100
	s_addc_u32 s49, s49, 0
	s_cmp_gt_u32 s45, 29
	s_cbranch_scc0 .LBB0_1460
